# P3 expert-weight conversion hand-written with 128k x 32n wave items: each store instruction writes full 128-byte lines of the transposed e4m3 rows; two item buffers
# speedup vs baseline: 1.0069x; 1.0069x over previous
; #define PHASE_ARGS() ArgsP AP = (ArgsP)__builtin_amdgcn_kernarg_segment_ptr(); asm volatile("" : "+s"(AP))
; #define PHASE_IDS() const int lane = (int)__builtin_amdgcn_mbcnt_hi(~0u, __builtin_amdgcn_mbcnt_lo(~0u, 0u)), wave = wave_s, tid = wave * 64 + lane, gtid = wg * NTHR + tid, gw = wg * NWAVES + wave; (void)gtid; (void)gw
; __device__ __forceinline__ bool titem_group(int& it, TItem& t, const float* W, size_t wstride, int nmat, int K, int N, const float* gain, float scale, void* WT, size_t tstride_bytes, int mode, int fp8) {
;     const int nblk = N / 64, per = (K / 64) * nblk, tot = per * nmat;
;     if (it >= tot) { it -= tot; return false; }
;     const int mat = it / per, r = it % per, k0 = 64 * (r / nblk), n0 = 64 * (r % nblk), esz = (fp8 == 1) ? 1 : 2;
;     const int drow0 = (mode == 0) ? n0 : (256 * (n0 / 128) + (n0 % 128) + (mode == 2 ? 128 : 0));
;     t.src = W + (size_t)mat * wstride + (size_t)k0 * N + n0; t.gain = gain ? gain + k0 : nullptr;
;     t.dst = (unsigned char*)WT + (size_t)mat * tstride_bytes + ((size_t)drow0 * K + k0) * esz; t.ldw = N; t.ldwt = K * esz; t.fp8 = fp8; t.scale = scale; return true;
; }
; __device__ __forceinline__ void titem_load(const TItem& t, f32x4 (&v)[2][8], f32x4 (&g)[2], int lane) {
;     const int n4 = lane & 7, kr = lane >> 3;
;     const float* gp = t.gain ? t.gain : t.src;
; #pragma unroll
;     for (int h = 0; h < 2; ++h)
; #pragma unroll
;         for (int i = 0; i < 8; ++i) v[h][i] = *(const f32x4*)(t.src + (size_t)(8 * kr + i) * t.ldw + 32 * h + 4 * n4);
;     g[0] = *(const f32x4*)(gp + 8 * kr); g[1] = *(const f32x4*)(gp + 8 * kr + 4);
; }
; __global__ void __launch_bounds__(NTHR, 2) fwd_kernel(Args args) {
;     ...
;     if (IN(3)) { PHASE_ARGS(); PHASE_IDS();
;         const int half = (wg >> 3) & 1;
;     ...
;         if (half == 1) { CONVERT_RANGE(0, NEXP_ITEMS); __syncthreads(); }
.LBB0_438:
	s_load_dwordx2 s[0:1], s[94:95], 0xe8
	s_waitcnt lgkmcnt(0)
	s_cmp_lt_i32 s0, 4
	s_cselect_b64 s[2:3], -1, 0
	s_cmp_gt_i32 s1, 3
	s_cselect_b64 s[0:1], -1, 0
	v_writelane_b32 v254, s2, 35
	s_and_b64 s[0:1], s[2:3], s[0:1]
	s_cmpk_lt_i32 s93, 0x100
	v_writelane_b32 v254, s3, 36
	s_cselect_b64 s[2:3], -1, 0
	v_writelane_b32 v254, s2, 37
	s_andn2_b64 vcc, exec, s[0:1]
	s_lshl_b32 s0, s85, 5
	v_writelane_b32 v254, s3, 38
	v_writelane_b32 v254, s0, 39
	s_cbranch_vccnz .LBB0_1083
	v_writelane_b32 v254, s97, 40
	s_bitcmp0_b32 s93, 3
	v_readlane_b32 s0, v254, 12
	s_cselect_b64 s[12:13], -1, 0
	v_readlane_b32 s1, v254, 13
	s_mov_b32 s4, s0
	s_cmp_lt_i32 s0, 0x15000
	s_cselect_b64 s[0:1], -1, 0
	s_cmpk_lt_i32 s4, 0x7000
	s_cselect_b64 s[2:3], -1, 0
	v_writelane_b32 v254, s2, 41
	s_cmpk_gt_i32 s4, 0x6fff
	v_mbcnt_lo_u32_b32 v0, -1, 0
	v_writelane_b32 v254, s3, 42
	s_cselect_b64 s[2:3], -1, 0
	v_writelane_b32 v254, s2, 43
	v_mbcnt_hi_u32_b32 v202, -1, v0
	v_cndmask_b32_e64 v0, 0, 1, s[0:1]
	v_writelane_b32 v254, s3, 44
	s_add_i32 s2, s4, 0xffff9000
	v_writelane_b32 v254, s2, 45
	s_mul_hi_i32 s2, s4, 0x92492493
	s_add_i32 s2, s2, s4
	s_lshr_b32 s3, s2, 31
	s_ashr_i32 s2, s2, 11
	s_add_i32 s3, s2, s3
	s_mul_i32 s2, s3, 0xe00
	s_sub_i32 s2, s4, s2
	s_mul_i32 s4, s2, 0x4925
	s_lshr_b32 s5, s4, 31
	s_ashr_i32 s4, s4, 21
	s_add_i32 s4, s4, s5
	s_mul_i32 s5, s4, 0x70
	s_sub_i32 s2, s2, s5
	s_sext_i32_i16 s5, s2
	s_bfe_u32 s6, s2, 0x10007
	s_lshl_b32 s10, s5, 6
	s_add_i32 s2, s2, s6
	s_bfe_u32 s5, s5, 0x70012
	s_bfe_i32 s2, s2, 0x80000
	s_add_i32 s5, s10, s5
	s_lshl_b32 s8, s4, 6
	s_sext_i32_i16 s2, s2
	s_and_b32 s5, s5, 0xff80
	s_lshl_b32 s2, s2, 7
	s_sub_i32 s5, s10, s5
	s_ashr_i32 s9, s8, 31
	s_and_b32 s2, s2, 0xffffff00
	s_sext_i32_i16 s5, s5
	v_writelane_b32 v254, s8, 46
	s_add_i32 s2, s2, s5
	s_ashr_i32 s11, s10, 31
	v_writelane_b32 v254, s9, 47
	s_mul_hi_i32 s69, s3, 0x3800000
	s_mul_i32 s70, s3, 0x3800000
	v_writelane_b32 v254, s10, 48
	s_mul_hi_i32 s65, s3, 0x1c00000
	s_mul_i32 s68, s3, 0x1c00000
	s_ashr_i32 s3, s2, 31
	v_writelane_b32 v254, s11, 49
	s_lshl_b64 s[2:3], s[2:3], 11
	v_writelane_b32 v254, s2, 50
	v_cmp_ne_u32_e64 s[0:1], 1, v0
	s_mul_i32 s71, s4, 0x1c0000
	v_writelane_b32 v254, s3, 51
	v_writelane_b32 v254, s12, 52
	s_mul_hi_i32 s72, s8, 0x7000
	s_mov_b64 s[66:67], s[94:95]
	v_writelane_b32 v254, s13, 53
	v_writelane_b32 v254, s0, 54
	s_and_b64 vcc, exec, s[12:13]
	s_nop 0
	v_writelane_b32 v254, s1, 55
	s_cbranch_vccnz .LBB0_580
	v_readlane_b32 s0, v254, 54
	v_readlane_b32 s1, v254, 55
	s_and_b64 vcc, exec, s[0:1]
	s_cbranch_vccnz .LBB0_579
	s_load_dwordx2 s[2:3], s[66:67], 0xb0
	s_load_dwordx2 s[4:5], s[66:67], 0xc0
	s_load_dwordx2 s[6:7], s[66:67], 0xc8
	s_load_dwordx2 s[8:9], s[66:67], 0xe0
	v_readlane_b32 s25, v254, 12
	v_mbcnt_lo_u32_b32 v239, -1, 0
	v_mbcnt_hi_u32_b32 v239, -1, v239
	v_and_b32_e32 v237, 7, v239
	v_lshrrev_b32_e32 v203, 3, v239
	v_mul_u32_u24_e32 v220, 0x70000, v203
	v_lshl_add_u32 v220, v237, 4, v220
	v_lshlrev_b32_e32 v221, 17, v203
	v_lshl_add_u32 v221, v237, 4, v221
	v_lshlrev_b32_e32 v222, 6, v203
	v_lshlrev_b32_e32 v223, 13, v237
	v_lshl_add_u32 v223, v203, 4, v223
	v_mul_u32_u24_e32 v224, 0x7000, v237
	v_lshl_add_u32 v224, v203, 4, v224
	v_mov_b32_e32 v225, 0x43e00000
	s_mov_b32 s33, 0xc3e00000
	s_waitcnt lgkmcnt(0)
	s_add_u32 s8, s8, 0xb000000
	s_addc_u32 s9, s9, 0
	s_mov_b32 s35, 0
	s_lshl_b32 s37, s35, 11
	s_add_i32 s37, s37, s25
	s_lshr_b32 s45, s37, 9
	s_mul_i32 s45, s45, 0x2493
	s_lshr_b32 s45, s45, 16
	s_mul_i32 s51, s45, 0xe00
	s_sub_i32 s50, s37, s51
	s_lshr_b32 s51, s50, 5
	s_mul_i32 s51, s51, 0x2493
	s_lshr_b32 s51, s51, 16
	s_mul_i32 s53, s51, 0xe0
	s_sub_i32 s52, s50, s53
	s_and_b32 s53, s45, 7
	s_lshr_b32 s60, s45, 3
	s_cmp_lg_u32 s60, 0
	s_cselect_b32 s46, s6, s4
	s_cselect_b32 s47, s7, s5
	s_mul_i32 s63, s53, 0x3800000
	s_add_u32 s46, s46, s63
	s_addc_u32 s47, s47, 0
	s_mul_i32 s63, s51, 0x380000
	s_lshl_b32 s37, s52, 7
	s_add_i32 s63, s63, s37
	s_add_u32 s46, s46, s63
	s_addc_u32 s47, s47, 0
	s_lshl_b32 s63, s51, 9
	s_add_u32 s48, s2, s63
	s_addc_u32 s49, s3, 0
	s_mul_i32 s63, s53, 0x1c00000
	s_lshr_b32 s37, s52, 2
	s_lshl_b32 s37, s37, 19
	s_add_i32 s63, s63, s37
	s_and_b32 s37, s52, 3
	s_lshl_b32 s37, s37, 16
	s_add_i32 s63, s63, s37
	s_lshl_b32 s37, s60, 18
	s_add_i32 s63, s63, s37
	s_lshl_b32 s37, s51, 7
	s_add_i32 s63, s63, s37
	s_add_u32 s38, s8, s63
	s_addc_u32 s39, s9, 0
	global_load_dwordx4 v[0:3], v220, s[46:47]
	v_add_u32_e32 v238, 0x7000, v220
	global_load_dwordx4 v[4:7], v238, s[46:47]
	v_add_u32_e32 v238, 0xe000, v220
	global_load_dwordx4 v[8:11], v238, s[46:47]
	v_add_u32_e32 v238, 0x15000, v220
	global_load_dwordx4 v[12:15], v238, s[46:47]
	v_add_u32_e32 v238, 0x1c000, v220
	global_load_dwordx4 v[16:19], v238, s[46:47]
	v_add_u32_e32 v238, 0x23000, v220
	global_load_dwordx4 v[20:23], v238, s[46:47]
	v_add_u32_e32 v238, 0x2a000, v220
	global_load_dwordx4 v[24:27], v238, s[46:47]
	v_add_u32_e32 v238, 0x31000, v220
	global_load_dwordx4 v[28:31], v238, s[46:47]
	v_add_u32_e32 v238, 0x38000, v220
	global_load_dwordx4 v[32:35], v238, s[46:47]
	v_add_u32_e32 v238, 0x3f000, v220
	global_load_dwordx4 v[36:39], v238, s[46:47]
	v_add_u32_e32 v238, 0x46000, v220
	global_load_dwordx4 v[40:43], v238, s[46:47]
	v_add_u32_e32 v238, 0x4d000, v220
	global_load_dwordx4 v[44:47], v238, s[46:47]
	v_add_u32_e32 v238, 0x54000, v220
	global_load_dwordx4 v[48:51], v238, s[46:47]
	v_add_u32_e32 v238, 0x5b000, v220
	global_load_dwordx4 v[52:55], v238, s[46:47]
	v_add_u32_e32 v238, 0x62000, v220
	global_load_dwordx4 v[56:59], v238, s[46:47]
	v_add_u32_e32 v238, 0x69000, v220
; __device__ __forceinline__ bool titem_group(int& it, TItem& t, const float* W, size_t wstride, int nmat, int K, int N, const float* gain, float scale, void* WT, size_t tstride_bytes, int mode, int fp8) {
;     const int nblk = N / 64, per = (K / 64) * nblk, tot = per * nmat;
;     if (it >= tot) { it -= tot; return false; }
;     const int mat = it / per, r = it % per, k0 = 64 * (r / nblk), n0 = 64 * (r % nblk), esz = (fp8 == 1) ? 1 : 2;
;     const int drow0 = (mode == 0) ? n0 : (256 * (n0 / 128) + (n0 % 128) + (mode == 2 ? 128 : 0));
;     t.src = W + (size_t)mat * wstride + (size_t)k0 * N + n0; t.gain = gain ? gain + k0 : nullptr;
;     t.dst = (unsigned char*)WT + (size_t)mat * tstride_bytes + ((size_t)drow0 * K + k0) * esz; t.ldw = N; t.ldwt = K * esz; t.fp8 = fp8; t.scale = scale; return true;
; }
; __device__ __forceinline__ void titem_load(const TItem& t, f32x4 (&v)[2][8], f32x4 (&g)[2], int lane) {
;     const int n4 = lane & 7, kr = lane >> 3;
;     const float* gp = t.gain ? t.gain : t.src;
; #pragma unroll
;     for (int h = 0; h < 2; ++h)
; #pragma unroll
;         for (int i = 0; i < 8; ++i) v[h][i] = *(const f32x4*)(t.src + (size_t)(8 * kr + i) * t.ldw + 32 * h + 4 * n4);
;     g[0] = *(const f32x4*)(gp + 8 * kr); g[1] = *(const f32x4*)(gp + 8 * kr + 4);
; }
; __device__ __forceinline__ void titem_process(const TItem& t, const f32x4 (&v)[2][8], const f32x4 (&g)[2], int lane) {
;     const int n4 = lane & 7, kr = lane >> 3;
;     float s[8];
; #pragma unroll
;     for (int j = 0; j < 8; ++j) s[j] = t.gain ? g[j >> 2][j & 3] * t.scale : t.scale;
;     if (t.fp8 == 1) {
; #pragma unroll
;         for (int h = 0; h < 2; ++h)
; #pragma unroll
;             for (int i = 0; i < 4; ++i) { u32x2 o; o.x = epi::pk4_fp8(v[h][0][i] * s[0], v[h][1][i] * s[1], v[h][2][i] * s[2], v[h][3][i] * s[3]); o.y = epi::pk4_fp8(v[h][4][i] * s[4], v[h][5][i] * s[5], v[h][6][i] * s[6], v[h][7][i] * s[7]);
;                 __builtin_nontemporal_store(o, (u32x2*)(t.dst + (size_t)(32 * h + 4 * n4 + i) * t.ldwt + 8 * kr)); }
	global_load_dwordx4 v[60:63], v238, s[46:47]
	global_load_dwordx4 v[128:131], v222, s[48:49]
	global_load_dwordx4 v[132:135], v222, s[48:49] offset:16
	global_load_dwordx4 v[136:139], v222, s[48:49] offset:32
	global_load_dwordx4 v[140:143], v222, s[48:49] offset:48
	s_mov_b32 s35, 1
	s_lshl_b32 s37, s35, 11
	s_add_i32 s37, s37, s25
	s_lshr_b32 s45, s37, 9
	s_mul_i32 s45, s45, 0x2493
	s_lshr_b32 s45, s45, 16
	s_mul_i32 s51, s45, 0xe00
	s_sub_i32 s50, s37, s51
	s_lshr_b32 s51, s50, 5
	s_mul_i32 s51, s51, 0x2493
	s_lshr_b32 s51, s51, 16
	s_mul_i32 s53, s51, 0xe0
	s_sub_i32 s52, s50, s53
	s_and_b32 s53, s45, 7
	s_lshr_b32 s60, s45, 3
	s_cmp_lg_u32 s60, 0
	s_cselect_b32 s46, s6, s4
	s_cselect_b32 s47, s7, s5
	s_mul_i32 s63, s53, 0x3800000
	s_add_u32 s46, s46, s63
	s_addc_u32 s47, s47, 0
	s_mul_i32 s63, s51, 0x380000
	s_lshl_b32 s37, s52, 7
	s_add_i32 s63, s63, s37
	s_add_u32 s46, s46, s63
	s_addc_u32 s47, s47, 0
	s_lshl_b32 s63, s51, 9
	s_add_u32 s48, s2, s63
	s_addc_u32 s49, s3, 0
	s_mul_i32 s63, s53, 0x1c00000
	s_lshr_b32 s37, s52, 2
	s_lshl_b32 s37, s37, 19
	s_add_i32 s63, s63, s37
	s_and_b32 s37, s52, 3
	s_lshl_b32 s37, s37, 16
	s_add_i32 s63, s63, s37
	s_lshl_b32 s37, s60, 18
	s_add_i32 s63, s63, s37
	s_lshl_b32 s37, s51, 7
	s_add_i32 s63, s63, s37
	s_add_u32 s40, s8, s63
	s_addc_u32 s41, s9, 0
	global_load_dwordx4 v[64:67], v220, s[46:47]
	v_add_u32_e32 v238, 0x7000, v220
	global_load_dwordx4 v[68:71], v238, s[46:47]
	v_add_u32_e32 v238, 0xe000, v220
	global_load_dwordx4 v[72:75], v238, s[46:47]
	v_add_u32_e32 v238, 0x15000, v220
	global_load_dwordx4 v[76:79], v238, s[46:47]
	v_add_u32_e32 v238, 0x1c000, v220
	global_load_dwordx4 v[80:83], v238, s[46:47]
	v_add_u32_e32 v238, 0x23000, v220
	global_load_dwordx4 v[84:87], v238, s[46:47]
	v_add_u32_e32 v238, 0x2a000, v220
	global_load_dwordx4 v[88:91], v238, s[46:47]
	v_add_u32_e32 v238, 0x31000, v220
	global_load_dwordx4 v[92:95], v238, s[46:47]
	v_add_u32_e32 v238, 0x38000, v220
	global_load_dwordx4 v[96:99], v238, s[46:47]
	v_add_u32_e32 v238, 0x3f000, v220
	global_load_dwordx4 v[100:103], v238, s[46:47]
	v_add_u32_e32 v238, 0x46000, v220
	global_load_dwordx4 v[104:107], v238, s[46:47]
	v_add_u32_e32 v238, 0x4d000, v220
	global_load_dwordx4 v[108:111], v238, s[46:47]
	v_add_u32_e32 v238, 0x54000, v220
	global_load_dwordx4 v[112:115], v238, s[46:47]
	v_add_u32_e32 v238, 0x5b000, v220
	global_load_dwordx4 v[116:119], v238, s[46:47]
	v_add_u32_e32 v238, 0x62000, v220
	global_load_dwordx4 v[120:123], v238, s[46:47]
	v_add_u32_e32 v238, 0x69000, v220
	global_load_dwordx4 v[124:127], v238, s[46:47]
	global_load_dwordx4 v[144:147], v222, s[48:49]
	global_load_dwordx4 v[148:151], v222, s[48:49] offset:16
	global_load_dwordx4 v[152:155], v222, s[48:49] offset:32
	global_load_dwordx4 v[156:159], v222, s[48:49] offset:48
	s_waitcnt vmcnt(20)
	v_mul_f32_e32 v160, 0x43800000, v128
	v_mul_f32_e32 v161, 0x43800000, v129
	v_mul_f32_e32 v162, 0x43800000, v130
	v_mul_f32_e32 v163, 0x43800000, v131
	v_mul_f32_e32 v164, 0x43800000, v132
	v_mul_f32_e32 v165, 0x43800000, v133
	v_mul_f32_e32 v166, 0x43800000, v134
	v_mul_f32_e32 v167, 0x43800000, v135
	v_mul_f32_e32 v168, 0x43800000, v136
	v_mul_f32_e32 v169, 0x43800000, v137
	v_mul_f32_e32 v170, 0x43800000, v138
	v_mul_f32_e32 v171, 0x43800000, v139
	v_mul_f32_e32 v172, 0x43800000, v140
	v_mul_f32_e32 v173, 0x43800000, v141
	v_mul_f32_e32 v174, 0x43800000, v142
	v_mul_f32_e32 v175, 0x43800000, v143
	v_pk_mul_f32 v[0:1], v[0:1], v[160:161] op_sel:[0,0] op_sel_hi:[1,0]
	v_pk_mul_f32 v[2:3], v[2:3], v[160:161] op_sel:[0,0] op_sel_hi:[1,0]
	v_pk_mul_f32 v[4:5], v[4:5], v[160:161] op_sel:[0,1] op_sel_hi:[1,1]
	v_pk_mul_f32 v[6:7], v[6:7], v[160:161] op_sel:[0,1] op_sel_hi:[1,1]
	v_pk_mul_f32 v[8:9], v[8:9], v[162:163] op_sel:[0,0] op_sel_hi:[1,0]
	v_pk_mul_f32 v[10:11], v[10:11], v[162:163] op_sel:[0,0] op_sel_hi:[1,0]
	v_pk_mul_f32 v[12:13], v[12:13], v[162:163] op_sel:[0,1] op_sel_hi:[1,1]
	v_pk_mul_f32 v[14:15], v[14:15], v[162:163] op_sel:[0,1] op_sel_hi:[1,1]
	v_pk_mul_f32 v[16:17], v[16:17], v[164:165] op_sel:[0,0] op_sel_hi:[1,0]
	v_pk_mul_f32 v[18:19], v[18:19], v[164:165] op_sel:[0,0] op_sel_hi:[1,0]
	v_pk_mul_f32 v[20:21], v[20:21], v[164:165] op_sel:[0,1] op_sel_hi:[1,1]
	v_pk_mul_f32 v[22:23], v[22:23], v[164:165] op_sel:[0,1] op_sel_hi:[1,1]
	v_pk_mul_f32 v[24:25], v[24:25], v[166:167] op_sel:[0,0] op_sel_hi:[1,0]
	v_pk_mul_f32 v[26:27], v[26:27], v[166:167] op_sel:[0,0] op_sel_hi:[1,0]
	v_pk_mul_f32 v[28:29], v[28:29], v[166:167] op_sel:[0,1] op_sel_hi:[1,1]
	v_pk_mul_f32 v[30:31], v[30:31], v[166:167] op_sel:[0,1] op_sel_hi:[1,1]
	v_pk_mul_f32 v[32:33], v[32:33], v[168:169] op_sel:[0,0] op_sel_hi:[1,0]
	v_pk_mul_f32 v[34:35], v[34:35], v[168:169] op_sel:[0,0] op_sel_hi:[1,0]
	v_pk_mul_f32 v[36:37], v[36:37], v[168:169] op_sel:[0,1] op_sel_hi:[1,1]
	v_pk_mul_f32 v[38:39], v[38:39], v[168:169] op_sel:[0,1] op_sel_hi:[1,1]
	v_pk_mul_f32 v[40:41], v[40:41], v[170:171] op_sel:[0,0] op_sel_hi:[1,0]
	v_pk_mul_f32 v[42:43], v[42:43], v[170:171] op_sel:[0,0] op_sel_hi:[1,0]
	v_pk_mul_f32 v[44:45], v[44:45], v[170:171] op_sel:[0,1] op_sel_hi:[1,1]
	v_pk_mul_f32 v[46:47], v[46:47], v[170:171] op_sel:[0,1] op_sel_hi:[1,1]
	v_pk_mul_f32 v[48:49], v[48:49], v[172:173] op_sel:[0,0] op_sel_hi:[1,0]
	v_pk_mul_f32 v[50:51], v[50:51], v[172:173] op_sel:[0,0] op_sel_hi:[1,0]
	v_pk_mul_f32 v[52:53], v[52:53], v[172:173] op_sel:[0,1] op_sel_hi:[1,1]
	v_pk_mul_f32 v[54:55], v[54:55], v[172:173] op_sel:[0,1] op_sel_hi:[1,1]
	v_pk_mul_f32 v[56:57], v[56:57], v[174:175] op_sel:[0,0] op_sel_hi:[1,0]
	v_pk_mul_f32 v[58:59], v[58:59], v[174:175] op_sel:[0,0] op_sel_hi:[1,0]
; __device__ __forceinline__ bool titem_group(int& it, TItem& t, const float* W, size_t wstride, int nmat, int K, int N, const float* gain, float scale, void* WT, size_t tstride_bytes, int mode, int fp8) {
;     const int nblk = N / 64, per = (K / 64) * nblk, tot = per * nmat;
;     if (it >= tot) { it -= tot; return false; }
;     const int mat = it / per, r = it % per, k0 = 64 * (r / nblk), n0 = 64 * (r % nblk), esz = (fp8 == 1) ? 1 : 2;
;     const int drow0 = (mode == 0) ? n0 : (256 * (n0 / 128) + (n0 % 128) + (mode == 2 ? 128 : 0));
;     t.src = W + (size_t)mat * wstride + (size_t)k0 * N + n0; t.gain = gain ? gain + k0 : nullptr;
;     t.dst = (unsigned char*)WT + (size_t)mat * tstride_bytes + ((size_t)drow0 * K + k0) * esz; t.ldw = N; t.ldwt = K * esz; t.fp8 = fp8; t.scale = scale; return true;
; }
; __device__ __forceinline__ void titem_load(const TItem& t, f32x4 (&v)[2][8], f32x4 (&g)[2], int lane) {
;     const int n4 = lane & 7, kr = lane >> 3;
;     const float* gp = t.gain ? t.gain : t.src;
; #pragma unroll
;     for (int h = 0; h < 2; ++h)
; #pragma unroll
;         for (int i = 0; i < 8; ++i) v[h][i] = *(const f32x4*)(t.src + (size_t)(8 * kr + i) * t.ldw + 32 * h + 4 * n4);
;     g[0] = *(const f32x4*)(gp + 8 * kr); g[1] = *(const f32x4*)(gp + 8 * kr + 4);
; }
; __device__ __forceinline__ void titem_process(const TItem& t, const f32x4 (&v)[2][8], const f32x4 (&g)[2], int lane) {
;     const int n4 = lane & 7, kr = lane >> 3;
;     float s[8];
; #pragma unroll
;     for (int j = 0; j < 8; ++j) s[j] = t.gain ? g[j >> 2][j & 3] * t.scale : t.scale;
;     if (t.fp8 == 1) {
; #pragma unroll
;         for (int h = 0; h < 2; ++h)
; #pragma unroll
;             for (int i = 0; i < 4; ++i) { u32x2 o; o.x = epi::pk4_fp8(v[h][0][i] * s[0], v[h][1][i] * s[1], v[h][2][i] * s[2], v[h][3][i] * s[3]); o.y = epi::pk4_fp8(v[h][4][i] * s[4], v[h][5][i] * s[5], v[h][6][i] * s[6], v[h][7][i] * s[7]);
;                 __builtin_nontemporal_store(o, (u32x2*)(t.dst + (size_t)(32 * h + 4 * n4 + i) * t.ldwt + 8 * kr)); }
	v_pk_mul_f32 v[60:61], v[60:61], v[174:175] op_sel:[0,1] op_sel_hi:[1,1]
	v_pk_mul_f32 v[62:63], v[62:63], v[174:175] op_sel:[0,1] op_sel_hi:[1,1]
	v_med3_f32 v0, v0, s33, v225
	v_med3_f32 v1, v1, s33, v225
	v_med3_f32 v2, v2, s33, v225
	v_med3_f32 v3, v3, s33, v225
	v_med3_f32 v4, v4, s33, v225
	v_med3_f32 v5, v5, s33, v225
	v_med3_f32 v6, v6, s33, v225
	v_med3_f32 v7, v7, s33, v225
	v_med3_f32 v8, v8, s33, v225
	v_med3_f32 v9, v9, s33, v225
	v_med3_f32 v10, v10, s33, v225
	v_med3_f32 v11, v11, s33, v225
	v_med3_f32 v12, v12, s33, v225
	v_med3_f32 v13, v13, s33, v225
	v_med3_f32 v14, v14, s33, v225
	v_med3_f32 v15, v15, s33, v225
	v_med3_f32 v16, v16, s33, v225
	v_med3_f32 v17, v17, s33, v225
	v_med3_f32 v18, v18, s33, v225
	v_med3_f32 v19, v19, s33, v225
	v_med3_f32 v20, v20, s33, v225
	v_med3_f32 v21, v21, s33, v225
	v_med3_f32 v22, v22, s33, v225
	v_med3_f32 v23, v23, s33, v225
	v_med3_f32 v24, v24, s33, v225
	v_med3_f32 v25, v25, s33, v225
	v_med3_f32 v26, v26, s33, v225
	v_med3_f32 v27, v27, s33, v225
	v_med3_f32 v28, v28, s33, v225
	v_med3_f32 v29, v29, s33, v225
	v_med3_f32 v30, v30, s33, v225
	v_med3_f32 v31, v31, s33, v225
	v_med3_f32 v32, v32, s33, v225
	v_med3_f32 v33, v33, s33, v225
	v_med3_f32 v34, v34, s33, v225
	v_med3_f32 v35, v35, s33, v225
	v_med3_f32 v36, v36, s33, v225
	v_med3_f32 v37, v37, s33, v225
	v_med3_f32 v38, v38, s33, v225
	v_med3_f32 v39, v39, s33, v225
	v_med3_f32 v40, v40, s33, v225
	v_med3_f32 v41, v41, s33, v225
	v_med3_f32 v42, v42, s33, v225
	v_med3_f32 v43, v43, s33, v225
	v_med3_f32 v44, v44, s33, v225
	v_med3_f32 v45, v45, s33, v225
	v_med3_f32 v46, v46, s33, v225
	v_med3_f32 v47, v47, s33, v225
	v_med3_f32 v48, v48, s33, v225
	v_med3_f32 v49, v49, s33, v225
	v_med3_f32 v50, v50, s33, v225
	v_med3_f32 v51, v51, s33, v225
	v_med3_f32 v52, v52, s33, v225
	v_med3_f32 v53, v53, s33, v225
	v_med3_f32 v54, v54, s33, v225
	v_med3_f32 v55, v55, s33, v225
	v_med3_f32 v56, v56, s33, v225
	v_med3_f32 v57, v57, s33, v225
	v_med3_f32 v58, v58, s33, v225
	v_med3_f32 v59, v59, s33, v225
	v_med3_f32 v60, v60, s33, v225
	v_med3_f32 v61, v61, s33, v225
	v_med3_f32 v62, v62, s33, v225
	v_med3_f32 v63, v63, s33, v225
	v_cvt_pk_fp8_f32 v226, v0, v4
	v_cvt_pk_fp8_f32 v227, v16, v20
	v_cvt_pk_fp8_f32 v228, v32, v36
	v_cvt_pk_fp8_f32 v229, v48, v52
	v_cvt_pk_fp8_f32 v226, v8, v12 op_sel:[0,0,1]
	v_cvt_pk_fp8_f32 v227, v24, v28 op_sel:[0,0,1]
	v_cvt_pk_fp8_f32 v228, v40, v44 op_sel:[0,0,1]
	v_cvt_pk_fp8_f32 v229, v56, v60 op_sel:[0,0,1]
	s_nop 0
	global_store_dwordx4 v223, v[226:229], s[38:39] nt
	v_cvt_pk_fp8_f32 v230, v1, v5
	v_cvt_pk_fp8_f32 v231, v17, v21
	v_cvt_pk_fp8_f32 v232, v33, v37
	v_cvt_pk_fp8_f32 v233, v49, v53
	v_cvt_pk_fp8_f32 v230, v9, v13 op_sel:[0,0,1]
	v_cvt_pk_fp8_f32 v231, v25, v29 op_sel:[0,0,1]
	v_cvt_pk_fp8_f32 v232, v41, v45 op_sel:[0,0,1]
	v_cvt_pk_fp8_f32 v233, v57, v61 op_sel:[0,0,1]
	v_add_u32_e32 v238, 0x800, v223
	global_store_dwordx4 v238, v[230:233], s[38:39] nt
	v_cvt_pk_fp8_f32 v226, v2, v6
	v_cvt_pk_fp8_f32 v227, v18, v22
	v_cvt_pk_fp8_f32 v228, v34, v38
	v_cvt_pk_fp8_f32 v229, v50, v54
	v_cvt_pk_fp8_f32 v226, v10, v14 op_sel:[0,0,1]
	v_cvt_pk_fp8_f32 v227, v26, v30 op_sel:[0,0,1]
	v_cvt_pk_fp8_f32 v228, v42, v46 op_sel:[0,0,1]
	v_cvt_pk_fp8_f32 v229, v58, v62 op_sel:[0,0,1]
	v_add_u32_e32 v238, 0x1000, v223
	global_store_dwordx4 v238, v[226:229], s[38:39] nt
	v_cvt_pk_fp8_f32 v230, v3, v7
	v_cvt_pk_fp8_f32 v231, v19, v23
	v_cvt_pk_fp8_f32 v232, v35, v39
	v_cvt_pk_fp8_f32 v233, v51, v55
	v_cvt_pk_fp8_f32 v230, v11, v15 op_sel:[0,0,1]
	v_cvt_pk_fp8_f32 v231, v27, v31 op_sel:[0,0,1]
	v_cvt_pk_fp8_f32 v232, v43, v47 op_sel:[0,0,1]
	v_cvt_pk_fp8_f32 v233, v59, v63 op_sel:[0,0,1]
	v_add_u32_e32 v238, 0x1800, v223
	global_store_dwordx4 v238, v[230:233], s[38:39] nt
	s_mov_b32 s27, 1
	s_mov_b32 s30, 14
.Lcv1_gu:
	s_add_i32 s35, s27, 1
	s_min_u32 s35, s35, 27
	s_lshl_b32 s37, s35, 11
	s_add_i32 s37, s37, s25
	s_lshr_b32 s45, s37, 9
	s_mul_i32 s45, s45, 0x2493
	s_lshr_b32 s45, s45, 16
	s_mul_i32 s51, s45, 0xe00
	s_sub_i32 s50, s37, s51
	s_lshr_b32 s51, s50, 5
	s_mul_i32 s51, s51, 0x2493
	s_lshr_b32 s51, s51, 16
	s_mul_i32 s53, s51, 0xe0
	s_sub_i32 s52, s50, s53
	s_and_b32 s53, s45, 7
	s_lshr_b32 s60, s45, 3
	s_cmp_lg_u32 s60, 0
	s_cselect_b32 s46, s6, s4
	s_cselect_b32 s47, s7, s5
	s_mul_i32 s63, s53, 0x3800000
	s_add_u32 s46, s46, s63
	s_addc_u32 s47, s47, 0
	s_mul_i32 s63, s51, 0x380000
	s_lshl_b32 s37, s52, 7
	s_add_i32 s63, s63, s37
	s_add_u32 s46, s46, s63
	s_addc_u32 s47, s47, 0
	s_lshl_b32 s63, s51, 9
	s_add_u32 s48, s2, s63
	s_addc_u32 s49, s3, 0
	s_mul_i32 s63, s53, 0x1c00000
	s_lshr_b32 s37, s52, 2
	s_lshl_b32 s37, s37, 19
	s_add_i32 s63, s63, s37
	s_and_b32 s37, s52, 3
	s_lshl_b32 s37, s37, 16
	s_add_i32 s63, s63, s37
	s_lshl_b32 s37, s60, 18
	s_add_i32 s63, s63, s37
	s_lshl_b32 s37, s51, 7
	s_add_i32 s63, s63, s37
	s_add_u32 s38, s8, s63
	s_addc_u32 s39, s9, 0
	global_load_dwordx4 v[0:3], v220, s[46:47]
	v_add_u32_e32 v238, 0x7000, v220
	global_load_dwordx4 v[4:7], v238, s[46:47]
	v_add_u32_e32 v238, 0xe000, v220
	global_load_dwordx4 v[8:11], v238, s[46:47]
	v_add_u32_e32 v238, 0x15000, v220
	global_load_dwordx4 v[12:15], v238, s[46:47]
	v_add_u32_e32 v238, 0x1c000, v220
	global_load_dwordx4 v[16:19], v238, s[46:47]
	v_add_u32_e32 v238, 0x23000, v220
	global_load_dwordx4 v[20:23], v238, s[46:47]
	v_add_u32_e32 v238, 0x2a000, v220
	global_load_dwordx4 v[24:27], v238, s[46:47]
	v_add_u32_e32 v238, 0x31000, v220
	global_load_dwordx4 v[28:31], v238, s[46:47]
	v_add_u32_e32 v238, 0x38000, v220
	global_load_dwordx4 v[32:35], v238, s[46:47]
	v_add_u32_e32 v238, 0x3f000, v220
	global_load_dwordx4 v[36:39], v238, s[46:47]
	v_add_u32_e32 v238, 0x46000, v220
	global_load_dwordx4 v[40:43], v238, s[46:47]
	v_add_u32_e32 v238, 0x4d000, v220
	global_load_dwordx4 v[44:47], v238, s[46:47]
	v_add_u32_e32 v238, 0x54000, v220
	global_load_dwordx4 v[48:51], v238, s[46:47]
	v_add_u32_e32 v238, 0x5b000, v220
	global_load_dwordx4 v[52:55], v238, s[46:47]
	v_add_u32_e32 v238, 0x62000, v220
	global_load_dwordx4 v[56:59], v238, s[46:47]
	v_add_u32_e32 v238, 0x69000, v220
	global_load_dwordx4 v[60:63], v238, s[46:47]
	global_load_dwordx4 v[128:131], v222, s[48:49]
	global_load_dwordx4 v[132:135], v222, s[48:49] offset:16
	global_load_dwordx4 v[136:139], v222, s[48:49] offset:32
	global_load_dwordx4 v[140:143], v222, s[48:49] offset:48
	s_waitcnt vmcnt(24)
; __device__ __forceinline__ unsigned pk4_fp8(float a, float b, float c, float d) {
;     a = __builtin_amdgcn_fmed3f(a, -448.f, 448.f); b = __builtin_amdgcn_fmed3f(b, -448.f, 448.f); c = __builtin_amdgcn_fmed3f(c, -448.f, 448.f); d = __builtin_amdgcn_fmed3f(d, -448.f, 448.f);
;     unsigned w = 0u; w = __builtin_amdgcn_cvt_pk_fp8_f32(a, b, w, false); w = __builtin_amdgcn_cvt_pk_fp8_f32(c, d, w, true); return w;
; }
; __device__ __forceinline__ void titem_process(const TItem& t, const f32x4 (&v)[2][8], const f32x4 (&g)[2], int lane) {
;     const int n4 = lane & 7, kr = lane >> 3;
;     float s[8];
; #pragma unroll
;     for (int j = 0; j < 8; ++j) s[j] = t.gain ? g[j >> 2][j & 3] * t.scale : t.scale;
;     if (t.fp8 == 1) {
; #pragma unroll
;         for (int h = 0; h < 2; ++h)
; #pragma unroll
;             for (int i = 0; i < 4; ++i) { u32x2 o; o.x = epi::pk4_fp8(v[h][0][i] * s[0], v[h][1][i] * s[1], v[h][2][i] * s[2], v[h][3][i] * s[3]); o.y = epi::pk4_fp8(v[h][4][i] * s[4], v[h][5][i] * s[5], v[h][6][i] * s[6], v[h][7][i] * s[7]);
;                 __builtin_nontemporal_store(o, (u32x2*)(t.dst + (size_t)(32 * h + 4 * n4 + i) * t.ldwt + 8 * kr)); }
	v_mul_f32_e32 v160, 0x43800000, v144
	v_mul_f32_e32 v161, 0x43800000, v145
	v_mul_f32_e32 v162, 0x43800000, v146
	v_mul_f32_e32 v163, 0x43800000, v147
	v_mul_f32_e32 v164, 0x43800000, v148
	v_mul_f32_e32 v165, 0x43800000, v149
	v_mul_f32_e32 v166, 0x43800000, v150
	v_mul_f32_e32 v167, 0x43800000, v151
	v_mul_f32_e32 v168, 0x43800000, v152
	v_mul_f32_e32 v169, 0x43800000, v153
	v_mul_f32_e32 v170, 0x43800000, v154
	v_mul_f32_e32 v171, 0x43800000, v155
	v_mul_f32_e32 v172, 0x43800000, v156
	v_mul_f32_e32 v173, 0x43800000, v157
	v_mul_f32_e32 v174, 0x43800000, v158
	v_mul_f32_e32 v175, 0x43800000, v159
	v_pk_mul_f32 v[64:65], v[64:65], v[160:161] op_sel:[0,0] op_sel_hi:[1,0]
	v_pk_mul_f32 v[66:67], v[66:67], v[160:161] op_sel:[0,0] op_sel_hi:[1,0]
	v_pk_mul_f32 v[68:69], v[68:69], v[160:161] op_sel:[0,1] op_sel_hi:[1,1]
	v_pk_mul_f32 v[70:71], v[70:71], v[160:161] op_sel:[0,1] op_sel_hi:[1,1]
	v_pk_mul_f32 v[72:73], v[72:73], v[162:163] op_sel:[0,0] op_sel_hi:[1,0]
	v_pk_mul_f32 v[74:75], v[74:75], v[162:163] op_sel:[0,0] op_sel_hi:[1,0]
	v_pk_mul_f32 v[76:77], v[76:77], v[162:163] op_sel:[0,1] op_sel_hi:[1,1]
	v_pk_mul_f32 v[78:79], v[78:79], v[162:163] op_sel:[0,1] op_sel_hi:[1,1]
	v_pk_mul_f32 v[80:81], v[80:81], v[164:165] op_sel:[0,0] op_sel_hi:[1,0]
	v_pk_mul_f32 v[82:83], v[82:83], v[164:165] op_sel:[0,0] op_sel_hi:[1,0]
	v_pk_mul_f32 v[84:85], v[84:85], v[164:165] op_sel:[0,1] op_sel_hi:[1,1]
	v_pk_mul_f32 v[86:87], v[86:87], v[164:165] op_sel:[0,1] op_sel_hi:[1,1]
	v_pk_mul_f32 v[88:89], v[88:89], v[166:167] op_sel:[0,0] op_sel_hi:[1,0]
	v_pk_mul_f32 v[90:91], v[90:91], v[166:167] op_sel:[0,0] op_sel_hi:[1,0]
	v_pk_mul_f32 v[92:93], v[92:93], v[166:167] op_sel:[0,1] op_sel_hi:[1,1]
	v_pk_mul_f32 v[94:95], v[94:95], v[166:167] op_sel:[0,1] op_sel_hi:[1,1]
	v_pk_mul_f32 v[96:97], v[96:97], v[168:169] op_sel:[0,0] op_sel_hi:[1,0]
	v_pk_mul_f32 v[98:99], v[98:99], v[168:169] op_sel:[0,0] op_sel_hi:[1,0]
	v_pk_mul_f32 v[100:101], v[100:101], v[168:169] op_sel:[0,1] op_sel_hi:[1,1]
	v_pk_mul_f32 v[102:103], v[102:103], v[168:169] op_sel:[0,1] op_sel_hi:[1,1]
	v_pk_mul_f32 v[104:105], v[104:105], v[170:171] op_sel:[0,0] op_sel_hi:[1,0]
	v_pk_mul_f32 v[106:107], v[106:107], v[170:171] op_sel:[0,0] op_sel_hi:[1,0]
	v_pk_mul_f32 v[108:109], v[108:109], v[170:171] op_sel:[0,1] op_sel_hi:[1,1]
	v_pk_mul_f32 v[110:111], v[110:111], v[170:171] op_sel:[0,1] op_sel_hi:[1,1]
	v_pk_mul_f32 v[112:113], v[112:113], v[172:173] op_sel:[0,0] op_sel_hi:[1,0]
	v_pk_mul_f32 v[114:115], v[114:115], v[172:173] op_sel:[0,0] op_sel_hi:[1,0]
	v_pk_mul_f32 v[116:117], v[116:117], v[172:173] op_sel:[0,1] op_sel_hi:[1,1]
	v_pk_mul_f32 v[118:119], v[118:119], v[172:173] op_sel:[0,1] op_sel_hi:[1,1]
	v_pk_mul_f32 v[120:121], v[120:121], v[174:175] op_sel:[0,0] op_sel_hi:[1,0]
	v_pk_mul_f32 v[122:123], v[122:123], v[174:175] op_sel:[0,0] op_sel_hi:[1,0]
	v_pk_mul_f32 v[124:125], v[124:125], v[174:175] op_sel:[0,1] op_sel_hi:[1,1]
	v_pk_mul_f32 v[126:127], v[126:127], v[174:175] op_sel:[0,1] op_sel_hi:[1,1]
	v_med3_f32 v64, v64, s33, v225
	v_med3_f32 v65, v65, s33, v225
	v_med3_f32 v66, v66, s33, v225
	v_med3_f32 v67, v67, s33, v225
	v_med3_f32 v68, v68, s33, v225
	v_med3_f32 v69, v69, s33, v225
	v_med3_f32 v70, v70, s33, v225
	v_med3_f32 v71, v71, s33, v225
	v_med3_f32 v72, v72, s33, v225
	v_med3_f32 v73, v73, s33, v225
	v_med3_f32 v74, v74, s33, v225
	v_med3_f32 v75, v75, s33, v225
	v_med3_f32 v76, v76, s33, v225
	v_med3_f32 v77, v77, s33, v225
	v_med3_f32 v78, v78, s33, v225
	v_med3_f32 v79, v79, s33, v225
	v_med3_f32 v80, v80, s33, v225
	v_med3_f32 v81, v81, s33, v225
	v_med3_f32 v82, v82, s33, v225
	v_med3_f32 v83, v83, s33, v225
	v_med3_f32 v84, v84, s33, v225
	v_med3_f32 v85, v85, s33, v225
	v_med3_f32 v86, v86, s33, v225
	v_med3_f32 v87, v87, s33, v225
	v_med3_f32 v88, v88, s33, v225
	v_med3_f32 v89, v89, s33, v225
	v_med3_f32 v90, v90, s33, v225
	v_med3_f32 v91, v91, s33, v225
	v_med3_f32 v92, v92, s33, v225
	v_med3_f32 v93, v93, s33, v225
	v_med3_f32 v94, v94, s33, v225
	v_med3_f32 v95, v95, s33, v225
	v_med3_f32 v96, v96, s33, v225
	v_med3_f32 v97, v97, s33, v225
	v_med3_f32 v98, v98, s33, v225
	v_med3_f32 v99, v99, s33, v225
	v_med3_f32 v100, v100, s33, v225
	v_med3_f32 v101, v101, s33, v225
	v_med3_f32 v102, v102, s33, v225
	v_med3_f32 v103, v103, s33, v225
	v_med3_f32 v104, v104, s33, v225
	v_med3_f32 v105, v105, s33, v225
	v_med3_f32 v106, v106, s33, v225
	v_med3_f32 v107, v107, s33, v225
	v_med3_f32 v108, v108, s33, v225
	v_med3_f32 v109, v109, s33, v225
	v_med3_f32 v110, v110, s33, v225
	v_med3_f32 v111, v111, s33, v225
	v_med3_f32 v112, v112, s33, v225
	v_med3_f32 v113, v113, s33, v225
	v_med3_f32 v114, v114, s33, v225
	v_med3_f32 v115, v115, s33, v225
	v_med3_f32 v116, v116, s33, v225
	v_med3_f32 v117, v117, s33, v225
	v_med3_f32 v118, v118, s33, v225
	v_med3_f32 v119, v119, s33, v225
	v_med3_f32 v120, v120, s33, v225
	v_med3_f32 v121, v121, s33, v225
	v_med3_f32 v122, v122, s33, v225
	v_med3_f32 v123, v123, s33, v225
	v_med3_f32 v124, v124, s33, v225
	v_med3_f32 v125, v125, s33, v225
	v_med3_f32 v126, v126, s33, v225
	v_med3_f32 v127, v127, s33, v225
	v_cvt_pk_fp8_f32 v226, v64, v68
	v_cvt_pk_fp8_f32 v227, v80, v84
	v_cvt_pk_fp8_f32 v228, v96, v100
	v_cvt_pk_fp8_f32 v229, v112, v116
	v_cvt_pk_fp8_f32 v226, v72, v76 op_sel:[0,0,1]
	v_cvt_pk_fp8_f32 v227, v88, v92 op_sel:[0,0,1]
	v_cvt_pk_fp8_f32 v228, v104, v108 op_sel:[0,0,1]
	v_cvt_pk_fp8_f32 v229, v120, v124 op_sel:[0,0,1]
	s_nop 0
	global_store_dwordx4 v223, v[226:229], s[40:41] nt
	v_cvt_pk_fp8_f32 v230, v65, v69
	v_cvt_pk_fp8_f32 v231, v81, v85
	v_cvt_pk_fp8_f32 v232, v97, v101
; __device__ __forceinline__ bool titem_group(int& it, TItem& t, const float* W, size_t wstride, int nmat, int K, int N, const float* gain, float scale, void* WT, size_t tstride_bytes, int mode, int fp8) {
;     const int nblk = N / 64, per = (K / 64) * nblk, tot = per * nmat;
;     if (it >= tot) { it -= tot; return false; }
;     const int mat = it / per, r = it % per, k0 = 64 * (r / nblk), n0 = 64 * (r % nblk), esz = (fp8 == 1) ? 1 : 2;
;     const int drow0 = (mode == 0) ? n0 : (256 * (n0 / 128) + (n0 % 128) + (mode == 2 ? 128 : 0));
;     t.src = W + (size_t)mat * wstride + (size_t)k0 * N + n0; t.gain = gain ? gain + k0 : nullptr;
;     t.dst = (unsigned char*)WT + (size_t)mat * tstride_bytes + ((size_t)drow0 * K + k0) * esz; t.ldw = N; t.ldwt = K * esz; t.fp8 = fp8; t.scale = scale; return true;
; }
; __device__ __forceinline__ void titem_load(const TItem& t, f32x4 (&v)[2][8], f32x4 (&g)[2], int lane) {
;     const int n4 = lane & 7, kr = lane >> 3;
;     const float* gp = t.gain ? t.gain : t.src;
; #pragma unroll
;     for (int h = 0; h < 2; ++h)
; #pragma unroll
;         for (int i = 0; i < 8; ++i) v[h][i] = *(const f32x4*)(t.src + (size_t)(8 * kr + i) * t.ldw + 32 * h + 4 * n4);
;     g[0] = *(const f32x4*)(gp + 8 * kr); g[1] = *(const f32x4*)(gp + 8 * kr + 4);
; }
; __device__ __forceinline__ void titem_process(const TItem& t, const f32x4 (&v)[2][8], const f32x4 (&g)[2], int lane) {
;     const int n4 = lane & 7, kr = lane >> 3;
;     float s[8];
; #pragma unroll
;     for (int j = 0; j < 8; ++j) s[j] = t.gain ? g[j >> 2][j & 3] * t.scale : t.scale;
;     if (t.fp8 == 1) {
; #pragma unroll
;         for (int h = 0; h < 2; ++h)
; #pragma unroll
;             for (int i = 0; i < 4; ++i) { u32x2 o; o.x = epi::pk4_fp8(v[h][0][i] * s[0], v[h][1][i] * s[1], v[h][2][i] * s[2], v[h][3][i] * s[3]); o.y = epi::pk4_fp8(v[h][4][i] * s[4], v[h][5][i] * s[5], v[h][6][i] * s[6], v[h][7][i] * s[7]);
;                 __builtin_nontemporal_store(o, (u32x2*)(t.dst + (size_t)(32 * h + 4 * n4 + i) * t.ldwt + 8 * kr)); }
	v_cvt_pk_fp8_f32 v233, v113, v117
	v_cvt_pk_fp8_f32 v230, v73, v77 op_sel:[0,0,1]
	v_cvt_pk_fp8_f32 v231, v89, v93 op_sel:[0,0,1]
	v_cvt_pk_fp8_f32 v232, v105, v109 op_sel:[0,0,1]
	v_cvt_pk_fp8_f32 v233, v121, v125 op_sel:[0,0,1]
	v_add_u32_e32 v238, 0x800, v223
	global_store_dwordx4 v238, v[230:233], s[40:41] nt
	v_cvt_pk_fp8_f32 v226, v66, v70
	v_cvt_pk_fp8_f32 v227, v82, v86
	v_cvt_pk_fp8_f32 v228, v98, v102
	v_cvt_pk_fp8_f32 v229, v114, v118
	v_cvt_pk_fp8_f32 v226, v74, v78 op_sel:[0,0,1]
	v_cvt_pk_fp8_f32 v227, v90, v94 op_sel:[0,0,1]
	v_cvt_pk_fp8_f32 v228, v106, v110 op_sel:[0,0,1]
	v_cvt_pk_fp8_f32 v229, v122, v126 op_sel:[0,0,1]
	v_add_u32_e32 v238, 0x1000, v223
	global_store_dwordx4 v238, v[226:229], s[40:41] nt
	v_cvt_pk_fp8_f32 v230, v67, v71
	v_cvt_pk_fp8_f32 v231, v83, v87
	v_cvt_pk_fp8_f32 v232, v99, v103
	v_cvt_pk_fp8_f32 v233, v115, v119
	v_cvt_pk_fp8_f32 v230, v75, v79 op_sel:[0,0,1]
	v_cvt_pk_fp8_f32 v231, v91, v95 op_sel:[0,0,1]
	v_cvt_pk_fp8_f32 v232, v107, v111 op_sel:[0,0,1]
	v_cvt_pk_fp8_f32 v233, v123, v127 op_sel:[0,0,1]
	v_add_u32_e32 v238, 0x1800, v223
	global_store_dwordx4 v238, v[230:233], s[40:41] nt
	s_add_i32 s35, s27, 2
	s_min_u32 s35, s35, 27
	s_lshl_b32 s37, s35, 11
	s_add_i32 s37, s37, s25
	s_lshr_b32 s45, s37, 9
	s_mul_i32 s45, s45, 0x2493
	s_lshr_b32 s45, s45, 16
	s_mul_i32 s51, s45, 0xe00
	s_sub_i32 s50, s37, s51
	s_lshr_b32 s51, s50, 5
	s_mul_i32 s51, s51, 0x2493
	s_lshr_b32 s51, s51, 16
	s_mul_i32 s53, s51, 0xe0
	s_sub_i32 s52, s50, s53
	s_and_b32 s53, s45, 7
	s_lshr_b32 s60, s45, 3
	s_cmp_lg_u32 s60, 0
	s_cselect_b32 s46, s6, s4
	s_cselect_b32 s47, s7, s5
	s_mul_i32 s63, s53, 0x3800000
	s_add_u32 s46, s46, s63
	s_addc_u32 s47, s47, 0
	s_mul_i32 s63, s51, 0x380000
	s_lshl_b32 s37, s52, 7
	s_add_i32 s63, s63, s37
	s_add_u32 s46, s46, s63
	s_addc_u32 s47, s47, 0
	s_lshl_b32 s63, s51, 9
	s_add_u32 s48, s2, s63
	s_addc_u32 s49, s3, 0
	s_mul_i32 s63, s53, 0x1c00000
	s_lshr_b32 s37, s52, 2
	s_lshl_b32 s37, s37, 19
	s_add_i32 s63, s63, s37
	s_and_b32 s37, s52, 3
	s_lshl_b32 s37, s37, 16
	s_add_i32 s63, s63, s37
	s_lshl_b32 s37, s60, 18
	s_add_i32 s63, s63, s37
	s_lshl_b32 s37, s51, 7
	s_add_i32 s63, s63, s37
	s_add_u32 s40, s8, s63
	s_addc_u32 s41, s9, 0
	global_load_dwordx4 v[64:67], v220, s[46:47]
	v_add_u32_e32 v238, 0x7000, v220
	global_load_dwordx4 v[68:71], v238, s[46:47]
	v_add_u32_e32 v238, 0xe000, v220
	global_load_dwordx4 v[72:75], v238, s[46:47]
	v_add_u32_e32 v238, 0x15000, v220
	global_load_dwordx4 v[76:79], v238, s[46:47]
	v_add_u32_e32 v238, 0x1c000, v220
	global_load_dwordx4 v[80:83], v238, s[46:47]
	v_add_u32_e32 v238, 0x23000, v220
	global_load_dwordx4 v[84:87], v238, s[46:47]
	v_add_u32_e32 v238, 0x2a000, v220
	global_load_dwordx4 v[88:91], v238, s[46:47]
	v_add_u32_e32 v238, 0x31000, v220
	global_load_dwordx4 v[92:95], v238, s[46:47]
	v_add_u32_e32 v238, 0x38000, v220
	global_load_dwordx4 v[96:99], v238, s[46:47]
	v_add_u32_e32 v238, 0x3f000, v220
	global_load_dwordx4 v[100:103], v238, s[46:47]
	v_add_u32_e32 v238, 0x46000, v220
	global_load_dwordx4 v[104:107], v238, s[46:47]
	v_add_u32_e32 v238, 0x4d000, v220
	global_load_dwordx4 v[108:111], v238, s[46:47]
	v_add_u32_e32 v238, 0x54000, v220
	global_load_dwordx4 v[112:115], v238, s[46:47]
	v_add_u32_e32 v238, 0x5b000, v220
	global_load_dwordx4 v[116:119], v238, s[46:47]
	v_add_u32_e32 v238, 0x62000, v220
	global_load_dwordx4 v[120:123], v238, s[46:47]
	v_add_u32_e32 v238, 0x69000, v220
	global_load_dwordx4 v[124:127], v238, s[46:47]
	global_load_dwordx4 v[144:147], v222, s[48:49]
	global_load_dwordx4 v[148:151], v222, s[48:49] offset:16
	global_load_dwordx4 v[152:155], v222, s[48:49] offset:32
	global_load_dwordx4 v[156:159], v222, s[48:49] offset:48
	s_waitcnt vmcnt(24)
	v_mul_f32_e32 v160, 0x43800000, v128
	v_mul_f32_e32 v161, 0x43800000, v129
	v_mul_f32_e32 v162, 0x43800000, v130
	v_mul_f32_e32 v163, 0x43800000, v131
	v_mul_f32_e32 v164, 0x43800000, v132
	v_mul_f32_e32 v165, 0x43800000, v133
	v_mul_f32_e32 v166, 0x43800000, v134
	v_mul_f32_e32 v167, 0x43800000, v135
	v_mul_f32_e32 v168, 0x43800000, v136
	v_mul_f32_e32 v169, 0x43800000, v137
	v_mul_f32_e32 v170, 0x43800000, v138
	v_mul_f32_e32 v171, 0x43800000, v139
	v_mul_f32_e32 v172, 0x43800000, v140
	v_mul_f32_e32 v173, 0x43800000, v141
	v_mul_f32_e32 v174, 0x43800000, v142
	v_mul_f32_e32 v175, 0x43800000, v143
	v_pk_mul_f32 v[0:1], v[0:1], v[160:161] op_sel:[0,0] op_sel_hi:[1,0]
	v_pk_mul_f32 v[2:3], v[2:3], v[160:161] op_sel:[0,0] op_sel_hi:[1,0]
	v_pk_mul_f32 v[4:5], v[4:5], v[160:161] op_sel:[0,1] op_sel_hi:[1,1]
	v_pk_mul_f32 v[6:7], v[6:7], v[160:161] op_sel:[0,1] op_sel_hi:[1,1]
	v_pk_mul_f32 v[8:9], v[8:9], v[162:163] op_sel:[0,0] op_sel_hi:[1,0]
	v_pk_mul_f32 v[10:11], v[10:11], v[162:163] op_sel:[0,0] op_sel_hi:[1,0]
	v_pk_mul_f32 v[12:13], v[12:13], v[162:163] op_sel:[0,1] op_sel_hi:[1,1]
	v_pk_mul_f32 v[14:15], v[14:15], v[162:163] op_sel:[0,1] op_sel_hi:[1,1]
	v_pk_mul_f32 v[16:17], v[16:17], v[164:165] op_sel:[0,0] op_sel_hi:[1,0]
	v_pk_mul_f32 v[18:19], v[18:19], v[164:165] op_sel:[0,0] op_sel_hi:[1,0]
	v_pk_mul_f32 v[20:21], v[20:21], v[164:165] op_sel:[0,1] op_sel_hi:[1,1]
	v_pk_mul_f32 v[22:23], v[22:23], v[164:165] op_sel:[0,1] op_sel_hi:[1,1]
	v_pk_mul_f32 v[24:25], v[24:25], v[166:167] op_sel:[0,0] op_sel_hi:[1,0]
	v_pk_mul_f32 v[26:27], v[26:27], v[166:167] op_sel:[0,0] op_sel_hi:[1,0]
	v_pk_mul_f32 v[28:29], v[28:29], v[166:167] op_sel:[0,1] op_sel_hi:[1,1]
	v_pk_mul_f32 v[30:31], v[30:31], v[166:167] op_sel:[0,1] op_sel_hi:[1,1]
	v_pk_mul_f32 v[32:33], v[32:33], v[168:169] op_sel:[0,0] op_sel_hi:[1,0]
	v_pk_mul_f32 v[34:35], v[34:35], v[168:169] op_sel:[0,0] op_sel_hi:[1,0]
; __device__ __forceinline__ void titem_process(const TItem& t, const f32x4 (&v)[2][8], const f32x4 (&g)[2], int lane) {
;     const int n4 = lane & 7, kr = lane >> 3;
;     float s[8];
; #pragma unroll
;     for (int j = 0; j < 8; ++j) s[j] = t.gain ? g[j >> 2][j & 3] * t.scale : t.scale;
;     if (t.fp8 == 1) {
; #pragma unroll
;         for (int h = 0; h < 2; ++h)
; #pragma unroll
;             for (int i = 0; i < 4; ++i) { u32x2 o; o.x = epi::pk4_fp8(v[h][0][i] * s[0], v[h][1][i] * s[1], v[h][2][i] * s[2], v[h][3][i] * s[3]); o.y = epi::pk4_fp8(v[h][4][i] * s[4], v[h][5][i] * s[5], v[h][6][i] * s[6], v[h][7][i] * s[7]);
;                 __builtin_nontemporal_store(o, (u32x2*)(t.dst + (size_t)(32 * h + 4 * n4 + i) * t.ldwt + 8 * kr)); }
	v_pk_mul_f32 v[36:37], v[36:37], v[168:169] op_sel:[0,1] op_sel_hi:[1,1]
	v_pk_mul_f32 v[38:39], v[38:39], v[168:169] op_sel:[0,1] op_sel_hi:[1,1]
	v_pk_mul_f32 v[40:41], v[40:41], v[170:171] op_sel:[0,0] op_sel_hi:[1,0]
	v_pk_mul_f32 v[42:43], v[42:43], v[170:171] op_sel:[0,0] op_sel_hi:[1,0]
	v_pk_mul_f32 v[44:45], v[44:45], v[170:171] op_sel:[0,1] op_sel_hi:[1,1]
	v_pk_mul_f32 v[46:47], v[46:47], v[170:171] op_sel:[0,1] op_sel_hi:[1,1]
	v_pk_mul_f32 v[48:49], v[48:49], v[172:173] op_sel:[0,0] op_sel_hi:[1,0]
	v_pk_mul_f32 v[50:51], v[50:51], v[172:173] op_sel:[0,0] op_sel_hi:[1,0]
	v_pk_mul_f32 v[52:53], v[52:53], v[172:173] op_sel:[0,1] op_sel_hi:[1,1]
	v_pk_mul_f32 v[54:55], v[54:55], v[172:173] op_sel:[0,1] op_sel_hi:[1,1]
	v_pk_mul_f32 v[56:57], v[56:57], v[174:175] op_sel:[0,0] op_sel_hi:[1,0]
	v_pk_mul_f32 v[58:59], v[58:59], v[174:175] op_sel:[0,0] op_sel_hi:[1,0]
	v_pk_mul_f32 v[60:61], v[60:61], v[174:175] op_sel:[0,1] op_sel_hi:[1,1]
	v_pk_mul_f32 v[62:63], v[62:63], v[174:175] op_sel:[0,1] op_sel_hi:[1,1]
	v_med3_f32 v0, v0, s33, v225
	v_med3_f32 v1, v1, s33, v225
	v_med3_f32 v2, v2, s33, v225
	v_med3_f32 v3, v3, s33, v225
	v_med3_f32 v4, v4, s33, v225
	v_med3_f32 v5, v5, s33, v225
	v_med3_f32 v6, v6, s33, v225
	v_med3_f32 v7, v7, s33, v225
	v_med3_f32 v8, v8, s33, v225
	v_med3_f32 v9, v9, s33, v225
	v_med3_f32 v10, v10, s33, v225
	v_med3_f32 v11, v11, s33, v225
	v_med3_f32 v12, v12, s33, v225
	v_med3_f32 v13, v13, s33, v225
	v_med3_f32 v14, v14, s33, v225
	v_med3_f32 v15, v15, s33, v225
	v_med3_f32 v16, v16, s33, v225
	v_med3_f32 v17, v17, s33, v225
	v_med3_f32 v18, v18, s33, v225
	v_med3_f32 v19, v19, s33, v225
	v_med3_f32 v20, v20, s33, v225
	v_med3_f32 v21, v21, s33, v225
	v_med3_f32 v22, v22, s33, v225
	v_med3_f32 v23, v23, s33, v225
	v_med3_f32 v24, v24, s33, v225
	v_med3_f32 v25, v25, s33, v225
	v_med3_f32 v26, v26, s33, v225
	v_med3_f32 v27, v27, s33, v225
	v_med3_f32 v28, v28, s33, v225
	v_med3_f32 v29, v29, s33, v225
	v_med3_f32 v30, v30, s33, v225
	v_med3_f32 v31, v31, s33, v225
	v_med3_f32 v32, v32, s33, v225
	v_med3_f32 v33, v33, s33, v225
	v_med3_f32 v34, v34, s33, v225
	v_med3_f32 v35, v35, s33, v225
	v_med3_f32 v36, v36, s33, v225
	v_med3_f32 v37, v37, s33, v225
	v_med3_f32 v38, v38, s33, v225
	v_med3_f32 v39, v39, s33, v225
	v_med3_f32 v40, v40, s33, v225
	v_med3_f32 v41, v41, s33, v225
	v_med3_f32 v42, v42, s33, v225
	v_med3_f32 v43, v43, s33, v225
	v_med3_f32 v44, v44, s33, v225
	v_med3_f32 v45, v45, s33, v225
	v_med3_f32 v46, v46, s33, v225
	v_med3_f32 v47, v47, s33, v225
	v_med3_f32 v48, v48, s33, v225
	v_med3_f32 v49, v49, s33, v225
	v_med3_f32 v50, v50, s33, v225
	v_med3_f32 v51, v51, s33, v225
	v_med3_f32 v52, v52, s33, v225
	v_med3_f32 v53, v53, s33, v225
	v_med3_f32 v54, v54, s33, v225
	v_med3_f32 v55, v55, s33, v225
	v_med3_f32 v56, v56, s33, v225
	v_med3_f32 v57, v57, s33, v225
	v_med3_f32 v58, v58, s33, v225
	v_med3_f32 v59, v59, s33, v225
	v_med3_f32 v60, v60, s33, v225
	v_med3_f32 v61, v61, s33, v225
	v_med3_f32 v62, v62, s33, v225
	v_med3_f32 v63, v63, s33, v225
	v_cvt_pk_fp8_f32 v226, v0, v4
	v_cvt_pk_fp8_f32 v227, v16, v20
	v_cvt_pk_fp8_f32 v228, v32, v36
	v_cvt_pk_fp8_f32 v229, v48, v52
	v_cvt_pk_fp8_f32 v226, v8, v12 op_sel:[0,0,1]
	v_cvt_pk_fp8_f32 v227, v24, v28 op_sel:[0,0,1]
	v_cvt_pk_fp8_f32 v228, v40, v44 op_sel:[0,0,1]
	v_cvt_pk_fp8_f32 v229, v56, v60 op_sel:[0,0,1]
	s_nop 0
	global_store_dwordx4 v223, v[226:229], s[38:39] nt
	v_cvt_pk_fp8_f32 v230, v1, v5
	v_cvt_pk_fp8_f32 v231, v17, v21
	v_cvt_pk_fp8_f32 v232, v33, v37
	v_cvt_pk_fp8_f32 v233, v49, v53
	v_cvt_pk_fp8_f32 v230, v9, v13 op_sel:[0,0,1]
	v_cvt_pk_fp8_f32 v231, v25, v29 op_sel:[0,0,1]
	v_cvt_pk_fp8_f32 v232, v41, v45 op_sel:[0,0,1]
	v_cvt_pk_fp8_f32 v233, v57, v61 op_sel:[0,0,1]
	v_add_u32_e32 v238, 0x800, v223
	global_store_dwordx4 v238, v[230:233], s[38:39] nt
	v_cvt_pk_fp8_f32 v226, v2, v6
	v_cvt_pk_fp8_f32 v227, v18, v22
	v_cvt_pk_fp8_f32 v228, v34, v38
	v_cvt_pk_fp8_f32 v229, v50, v54
	v_cvt_pk_fp8_f32 v226, v10, v14 op_sel:[0,0,1]
	v_cvt_pk_fp8_f32 v227, v26, v30 op_sel:[0,0,1]
	v_cvt_pk_fp8_f32 v228, v42, v46 op_sel:[0,0,1]
	v_cvt_pk_fp8_f32 v229, v58, v62 op_sel:[0,0,1]
	v_add_u32_e32 v238, 0x1000, v223
	global_store_dwordx4 v238, v[226:229], s[38:39] nt
	v_cvt_pk_fp8_f32 v230, v3, v7
	v_cvt_pk_fp8_f32 v231, v19, v23
	v_cvt_pk_fp8_f32 v232, v35, v39
	v_cvt_pk_fp8_f32 v233, v51, v55
	v_cvt_pk_fp8_f32 v230, v11, v15 op_sel:[0,0,1]
	v_cvt_pk_fp8_f32 v231, v27, v31 op_sel:[0,0,1]
	v_cvt_pk_fp8_f32 v232, v43, v47 op_sel:[0,0,1]
	v_cvt_pk_fp8_f32 v233, v59, v63 op_sel:[0,0,1]
	v_add_u32_e32 v238, 0x1800, v223
	global_store_dwordx4 v238, v[230:233], s[38:39] nt
	s_add_i32 s27, s27, 2
	s_sub_i32 s30, s30, 1
	s_cmp_lg_u32 s30, 0
	s_cbranch_scc1 .Lcv1_gu
; __device__ __forceinline__ bool titem_group(int& it, TItem& t, const float* W, size_t wstride, int nmat, int K, int N, const float* gain, float scale, void* WT, size_t tstride_bytes, int mode, int fp8) {
;     const int nblk = N / 64, per = (K / 64) * nblk, tot = per * nmat;
;     if (it >= tot) { it -= tot; return false; }
;     const int mat = it / per, r = it % per, k0 = 64 * (r / nblk), n0 = 64 * (r % nblk), esz = (fp8 == 1) ? 1 : 2;
;     const int drow0 = (mode == 0) ? n0 : (256 * (n0 / 128) + (n0 % 128) + (mode == 2 ? 128 : 0));
;     t.src = W + (size_t)mat * wstride + (size_t)k0 * N + n0; t.gain = gain ? gain + k0 : nullptr;
;     t.dst = (unsigned char*)WT + (size_t)mat * tstride_bytes + ((size_t)drow0 * K + k0) * esz; t.ldw = N; t.ldwt = K * esz; t.fp8 = fp8; t.scale = scale; return true;
; }
; __device__ __forceinline__ void titem_load(const TItem& t, f32x4 (&v)[2][8], f32x4 (&g)[2], int lane) {
;     const int n4 = lane & 7, kr = lane >> 3;
;     const float* gp = t.gain ? t.gain : t.src;
; #pragma unroll
;     for (int h = 0; h < 2; ++h)
; #pragma unroll
;         for (int i = 0; i < 8; ++i) v[h][i] = *(const f32x4*)(t.src + (size_t)(8 * kr + i) * t.ldw + 32 * h + 4 * n4);
;     g[0] = *(const f32x4*)(gp + 8 * kr); g[1] = *(const f32x4*)(gp + 8 * kr + 4);
; }
	s_waitcnt vmcnt(0)
	s_load_dwordx2 s[4:5], s[66:67], 0xd0
	s_load_dwordx2 s[8:9], s[66:67], 0xe0
	s_waitcnt lgkmcnt(0)
	s_add_u32 s8, s8, 0x27000000
	s_addc_u32 s9, s9, 0
	s_mov_b32 s35, 0
	s_lshl_b32 s37, s35, 11
	s_add_i32 s37, s37, s25
	s_lshr_b32 s45, s37, 9
	s_mul_i32 s45, s45, 0x2493
	s_lshr_b32 s45, s45, 16
	s_mul_i32 s51, s45, 0xe00
	s_sub_i32 s50, s37, s51
	s_lshr_b32 s51, s50, 6
	s_and_b32 s52, s50, 63
	s_mul_i32 s63, s45, 0x3800000
	s_add_u32 s46, s4, s63
	s_addc_u32 s47, s5, 0
	s_lshl_b32 s63, s51, 20
	s_lshl_b32 s37, s52, 7
	s_add_i32 s63, s63, s37
	s_add_u32 s46, s46, s63
	s_addc_u32 s47, s47, 0
	s_mov_b64 s[48:49], s[4:5]
	s_mul_i32 s63, s45, 0xe00000
	s_mul_i32 s37, s52, 0x38000
	s_add_i32 s63, s63, s37
	s_lshl_b32 s37, s51, 7
	s_add_i32 s63, s63, s37
	s_add_u32 s38, s8, s63
	s_addc_u32 s39, s9, 0
	global_load_dwordx4 v[0:3], v221, s[46:47]
	v_add_u32_e32 v238, 0x2000, v221
	global_load_dwordx4 v[4:7], v238, s[46:47]
	v_add_u32_e32 v238, 0x4000, v221
	global_load_dwordx4 v[8:11], v238, s[46:47]
	v_add_u32_e32 v238, 0x6000, v221
	global_load_dwordx4 v[12:15], v238, s[46:47]
	v_add_u32_e32 v238, 0x8000, v221
	global_load_dwordx4 v[16:19], v238, s[46:47]
	v_add_u32_e32 v238, 0xa000, v221
	global_load_dwordx4 v[20:23], v238, s[46:47]
	v_add_u32_e32 v238, 0xc000, v221
	global_load_dwordx4 v[24:27], v238, s[46:47]
	v_add_u32_e32 v238, 0xe000, v221
	global_load_dwordx4 v[28:31], v238, s[46:47]
	v_add_u32_e32 v238, 0x10000, v221
	global_load_dwordx4 v[32:35], v238, s[46:47]
	v_add_u32_e32 v238, 0x12000, v221
	global_load_dwordx4 v[36:39], v238, s[46:47]
	v_add_u32_e32 v238, 0x14000, v221
	global_load_dwordx4 v[40:43], v238, s[46:47]
	v_add_u32_e32 v238, 0x16000, v221
	global_load_dwordx4 v[44:47], v238, s[46:47]
	v_add_u32_e32 v238, 0x18000, v221
	global_load_dwordx4 v[48:51], v238, s[46:47]
	v_add_u32_e32 v238, 0x1a000, v221
	global_load_dwordx4 v[52:55], v238, s[46:47]
	v_add_u32_e32 v238, 0x1c000, v221
	global_load_dwordx4 v[56:59], v238, s[46:47]
	v_add_u32_e32 v238, 0x1e000, v221
	global_load_dwordx4 v[60:63], v238, s[46:47]
	global_load_dwordx4 v[128:131], v222, s[48:49]
	global_load_dwordx4 v[132:135], v222, s[48:49] offset:16
	global_load_dwordx4 v[136:139], v222, s[48:49] offset:32
	global_load_dwordx4 v[140:143], v222, s[48:49] offset:48
	s_mov_b32 s35, 1
	s_lshl_b32 s37, s35, 11
	s_add_i32 s37, s37, s25
	s_lshr_b32 s45, s37, 9
	s_mul_i32 s45, s45, 0x2493
	s_lshr_b32 s45, s45, 16
	s_mul_i32 s51, s45, 0xe00
	s_sub_i32 s50, s37, s51
	s_lshr_b32 s51, s50, 6
	s_and_b32 s52, s50, 63
	s_mul_i32 s63, s45, 0x3800000
	s_add_u32 s46, s4, s63
	s_addc_u32 s47, s5, 0
	s_lshl_b32 s63, s51, 20
	s_lshl_b32 s37, s52, 7
	s_add_i32 s63, s63, s37
	s_add_u32 s46, s46, s63
	s_addc_u32 s47, s47, 0
	s_mov_b64 s[48:49], s[4:5]
	s_mul_i32 s63, s45, 0xe00000
	s_mul_i32 s37, s52, 0x38000
	s_add_i32 s63, s63, s37
	s_lshl_b32 s37, s51, 7
	s_add_i32 s63, s63, s37
	s_add_u32 s40, s8, s63
	s_addc_u32 s41, s9, 0
	global_load_dwordx4 v[64:67], v221, s[46:47]
	v_add_u32_e32 v238, 0x2000, v221
	global_load_dwordx4 v[68:71], v238, s[46:47]
	v_add_u32_e32 v238, 0x4000, v221
	global_load_dwordx4 v[72:75], v238, s[46:47]
	v_add_u32_e32 v238, 0x6000, v221
	global_load_dwordx4 v[76:79], v238, s[46:47]
	v_add_u32_e32 v238, 0x8000, v221
	global_load_dwordx4 v[80:83], v238, s[46:47]
	v_add_u32_e32 v238, 0xa000, v221
	global_load_dwordx4 v[84:87], v238, s[46:47]
	v_add_u32_e32 v238, 0xc000, v221
	global_load_dwordx4 v[88:91], v238, s[46:47]
	v_add_u32_e32 v238, 0xe000, v221
	global_load_dwordx4 v[92:95], v238, s[46:47]
	v_add_u32_e32 v238, 0x10000, v221
	global_load_dwordx4 v[96:99], v238, s[46:47]
	v_add_u32_e32 v238, 0x12000, v221
	global_load_dwordx4 v[100:103], v238, s[46:47]
	v_add_u32_e32 v238, 0x14000, v221
	global_load_dwordx4 v[104:107], v238, s[46:47]
	v_add_u32_e32 v238, 0x16000, v221
	global_load_dwordx4 v[108:111], v238, s[46:47]
	v_add_u32_e32 v238, 0x18000, v221
	global_load_dwordx4 v[112:115], v238, s[46:47]
	v_add_u32_e32 v238, 0x1a000, v221
	global_load_dwordx4 v[116:119], v238, s[46:47]
	v_add_u32_e32 v238, 0x1c000, v221
	global_load_dwordx4 v[120:123], v238, s[46:47]
	v_add_u32_e32 v238, 0x1e000, v221
	global_load_dwordx4 v[124:127], v238, s[46:47]
	global_load_dwordx4 v[144:147], v222, s[48:49]
	global_load_dwordx4 v[148:151], v222, s[48:49] offset:16
	global_load_dwordx4 v[152:155], v222, s[48:49] offset:32
	global_load_dwordx4 v[156:159], v222, s[48:49] offset:48
	s_waitcnt vmcnt(20)
; __device__ __forceinline__ unsigned pk4_fp8(float a, float b, float c, float d) {
;     a = __builtin_amdgcn_fmed3f(a, -448.f, 448.f); b = __builtin_amdgcn_fmed3f(b, -448.f, 448.f); c = __builtin_amdgcn_fmed3f(c, -448.f, 448.f); d = __builtin_amdgcn_fmed3f(d, -448.f, 448.f);
;     unsigned w = 0u; w = __builtin_amdgcn_cvt_pk_fp8_f32(a, b, w, false); w = __builtin_amdgcn_cvt_pk_fp8_f32(c, d, w, true); return w;
; }
; __device__ __forceinline__ void titem_process(const TItem& t, const f32x4 (&v)[2][8], const f32x4 (&g)[2], int lane) {
;     const int n4 = lane & 7, kr = lane >> 3;
;     float s[8];
; #pragma unroll
;     for (int j = 0; j < 8; ++j) s[j] = t.gain ? g[j >> 2][j & 3] * t.scale : t.scale;
;     if (t.fp8 == 1) {
; #pragma unroll
;         for (int h = 0; h < 2; ++h)
; #pragma unroll
;             for (int i = 0; i < 4; ++i) { u32x2 o; o.x = epi::pk4_fp8(v[h][0][i] * s[0], v[h][1][i] * s[1], v[h][2][i] * s[2], v[h][3][i] * s[3]); o.y = epi::pk4_fp8(v[h][4][i] * s[4], v[h][5][i] * s[5], v[h][6][i] * s[6], v[h][7][i] * s[7]);
;                 __builtin_nontemporal_store(o, (u32x2*)(t.dst + (size_t)(32 * h + 4 * n4 + i) * t.ldwt + 8 * kr)); }
	v_mov_b32_e32 v160, 0x44000000
	v_mov_b32_e32 v161, 0x44000000
	v_mov_b32_e32 v162, 0x44000000
	v_mov_b32_e32 v163, 0x44000000
	v_mov_b32_e32 v164, 0x44000000
	v_mov_b32_e32 v165, 0x44000000
	v_mov_b32_e32 v166, 0x44000000
	v_mov_b32_e32 v167, 0x44000000
	v_mov_b32_e32 v168, 0x44000000
	v_mov_b32_e32 v169, 0x44000000
	v_mov_b32_e32 v170, 0x44000000
	v_mov_b32_e32 v171, 0x44000000
	v_mov_b32_e32 v172, 0x44000000
	v_mov_b32_e32 v173, 0x44000000
	v_mov_b32_e32 v174, 0x44000000
	v_mov_b32_e32 v175, 0x44000000
	v_pk_mul_f32 v[0:1], v[0:1], v[160:161] op_sel:[0,0] op_sel_hi:[1,0]
	v_pk_mul_f32 v[2:3], v[2:3], v[160:161] op_sel:[0,0] op_sel_hi:[1,0]
	v_pk_mul_f32 v[4:5], v[4:5], v[160:161] op_sel:[0,1] op_sel_hi:[1,1]
	v_pk_mul_f32 v[6:7], v[6:7], v[160:161] op_sel:[0,1] op_sel_hi:[1,1]
	v_pk_mul_f32 v[8:9], v[8:9], v[162:163] op_sel:[0,0] op_sel_hi:[1,0]
	v_pk_mul_f32 v[10:11], v[10:11], v[162:163] op_sel:[0,0] op_sel_hi:[1,0]
	v_pk_mul_f32 v[12:13], v[12:13], v[162:163] op_sel:[0,1] op_sel_hi:[1,1]
	v_pk_mul_f32 v[14:15], v[14:15], v[162:163] op_sel:[0,1] op_sel_hi:[1,1]
	v_pk_mul_f32 v[16:17], v[16:17], v[164:165] op_sel:[0,0] op_sel_hi:[1,0]
	v_pk_mul_f32 v[18:19], v[18:19], v[164:165] op_sel:[0,0] op_sel_hi:[1,0]
	v_pk_mul_f32 v[20:21], v[20:21], v[164:165] op_sel:[0,1] op_sel_hi:[1,1]
	v_pk_mul_f32 v[22:23], v[22:23], v[164:165] op_sel:[0,1] op_sel_hi:[1,1]
	v_pk_mul_f32 v[24:25], v[24:25], v[166:167] op_sel:[0,0] op_sel_hi:[1,0]
	v_pk_mul_f32 v[26:27], v[26:27], v[166:167] op_sel:[0,0] op_sel_hi:[1,0]
	v_pk_mul_f32 v[28:29], v[28:29], v[166:167] op_sel:[0,1] op_sel_hi:[1,1]
	v_pk_mul_f32 v[30:31], v[30:31], v[166:167] op_sel:[0,1] op_sel_hi:[1,1]
	v_pk_mul_f32 v[32:33], v[32:33], v[168:169] op_sel:[0,0] op_sel_hi:[1,0]
	v_pk_mul_f32 v[34:35], v[34:35], v[168:169] op_sel:[0,0] op_sel_hi:[1,0]
	v_pk_mul_f32 v[36:37], v[36:37], v[168:169] op_sel:[0,1] op_sel_hi:[1,1]
	v_pk_mul_f32 v[38:39], v[38:39], v[168:169] op_sel:[0,1] op_sel_hi:[1,1]
	v_pk_mul_f32 v[40:41], v[40:41], v[170:171] op_sel:[0,0] op_sel_hi:[1,0]
	v_pk_mul_f32 v[42:43], v[42:43], v[170:171] op_sel:[0,0] op_sel_hi:[1,0]
	v_pk_mul_f32 v[44:45], v[44:45], v[170:171] op_sel:[0,1] op_sel_hi:[1,1]
	v_pk_mul_f32 v[46:47], v[46:47], v[170:171] op_sel:[0,1] op_sel_hi:[1,1]
	v_pk_mul_f32 v[48:49], v[48:49], v[172:173] op_sel:[0,0] op_sel_hi:[1,0]
	v_pk_mul_f32 v[50:51], v[50:51], v[172:173] op_sel:[0,0] op_sel_hi:[1,0]
	v_pk_mul_f32 v[52:53], v[52:53], v[172:173] op_sel:[0,1] op_sel_hi:[1,1]
	v_pk_mul_f32 v[54:55], v[54:55], v[172:173] op_sel:[0,1] op_sel_hi:[1,1]
	v_pk_mul_f32 v[56:57], v[56:57], v[174:175] op_sel:[0,0] op_sel_hi:[1,0]
	v_pk_mul_f32 v[58:59], v[58:59], v[174:175] op_sel:[0,0] op_sel_hi:[1,0]
	v_pk_mul_f32 v[60:61], v[60:61], v[174:175] op_sel:[0,1] op_sel_hi:[1,1]
	v_pk_mul_f32 v[62:63], v[62:63], v[174:175] op_sel:[0,1] op_sel_hi:[1,1]
	v_med3_f32 v0, v0, s33, v225
	v_med3_f32 v1, v1, s33, v225
	v_med3_f32 v2, v2, s33, v225
	v_med3_f32 v3, v3, s33, v225
	v_med3_f32 v4, v4, s33, v225
	v_med3_f32 v5, v5, s33, v225
	v_med3_f32 v6, v6, s33, v225
	v_med3_f32 v7, v7, s33, v225
	v_med3_f32 v8, v8, s33, v225
	v_med3_f32 v9, v9, s33, v225
	v_med3_f32 v10, v10, s33, v225
	v_med3_f32 v11, v11, s33, v225
	v_med3_f32 v12, v12, s33, v225
	v_med3_f32 v13, v13, s33, v225
	v_med3_f32 v14, v14, s33, v225
	v_med3_f32 v15, v15, s33, v225
	v_med3_f32 v16, v16, s33, v225
	v_med3_f32 v17, v17, s33, v225
	v_med3_f32 v18, v18, s33, v225
	v_med3_f32 v19, v19, s33, v225
	v_med3_f32 v20, v20, s33, v225
	v_med3_f32 v21, v21, s33, v225
	v_med3_f32 v22, v22, s33, v225
	v_med3_f32 v23, v23, s33, v225
	v_med3_f32 v24, v24, s33, v225
	v_med3_f32 v25, v25, s33, v225
	v_med3_f32 v26, v26, s33, v225
	v_med3_f32 v27, v27, s33, v225
	v_med3_f32 v28, v28, s33, v225
	v_med3_f32 v29, v29, s33, v225
	v_med3_f32 v30, v30, s33, v225
	v_med3_f32 v31, v31, s33, v225
	v_med3_f32 v32, v32, s33, v225
	v_med3_f32 v33, v33, s33, v225
	v_med3_f32 v34, v34, s33, v225
	v_med3_f32 v35, v35, s33, v225
	v_med3_f32 v36, v36, s33, v225
	v_med3_f32 v37, v37, s33, v225
	v_med3_f32 v38, v38, s33, v225
	v_med3_f32 v39, v39, s33, v225
	v_med3_f32 v40, v40, s33, v225
	v_med3_f32 v41, v41, s33, v225
	v_med3_f32 v42, v42, s33, v225
	v_med3_f32 v43, v43, s33, v225
	v_med3_f32 v44, v44, s33, v225
	v_med3_f32 v45, v45, s33, v225
	v_med3_f32 v46, v46, s33, v225
	v_med3_f32 v47, v47, s33, v225
	v_med3_f32 v48, v48, s33, v225
	v_med3_f32 v49, v49, s33, v225
	v_med3_f32 v50, v50, s33, v225
	v_med3_f32 v51, v51, s33, v225
	v_med3_f32 v52, v52, s33, v225
	v_med3_f32 v53, v53, s33, v225
	v_med3_f32 v54, v54, s33, v225
	v_med3_f32 v55, v55, s33, v225
	v_med3_f32 v56, v56, s33, v225
	v_med3_f32 v57, v57, s33, v225
	v_med3_f32 v58, v58, s33, v225
	v_med3_f32 v59, v59, s33, v225
	v_med3_f32 v60, v60, s33, v225
	v_med3_f32 v61, v61, s33, v225
	v_med3_f32 v62, v62, s33, v225
	v_med3_f32 v63, v63, s33, v225
	v_cvt_pk_fp8_f32 v226, v0, v4
	v_cvt_pk_fp8_f32 v227, v16, v20
	v_cvt_pk_fp8_f32 v228, v32, v36
	v_cvt_pk_fp8_f32 v229, v48, v52
	v_cvt_pk_fp8_f32 v226, v8, v12 op_sel:[0,0,1]
	v_cvt_pk_fp8_f32 v227, v24, v28 op_sel:[0,0,1]
	v_cvt_pk_fp8_f32 v228, v40, v44 op_sel:[0,0,1]
	v_cvt_pk_fp8_f32 v229, v56, v60 op_sel:[0,0,1]
	s_nop 0
	global_store_dwordx4 v224, v[226:229], s[38:39] nt
	v_cvt_pk_fp8_f32 v230, v1, v5
	v_cvt_pk_fp8_f32 v231, v17, v21
	v_cvt_pk_fp8_f32 v232, v33, v37
	v_cvt_pk_fp8_f32 v233, v49, v53
	v_cvt_pk_fp8_f32 v230, v9, v13 op_sel:[0,0,1]
	v_cvt_pk_fp8_f32 v231, v25, v29 op_sel:[0,0,1]
	v_cvt_pk_fp8_f32 v232, v41, v45 op_sel:[0,0,1]
	v_cvt_pk_fp8_f32 v233, v57, v61 op_sel:[0,0,1]
	v_add_u32_e32 v238, 0x1c00, v224
	global_store_dwordx4 v238, v[230:233], s[38:39] nt
	v_cvt_pk_fp8_f32 v226, v2, v6
	v_cvt_pk_fp8_f32 v227, v18, v22
	v_cvt_pk_fp8_f32 v228, v34, v38
	v_cvt_pk_fp8_f32 v229, v50, v54
	v_cvt_pk_fp8_f32 v226, v10, v14 op_sel:[0,0,1]
	v_cvt_pk_fp8_f32 v227, v26, v30 op_sel:[0,0,1]
	v_cvt_pk_fp8_f32 v228, v42, v46 op_sel:[0,0,1]
	v_cvt_pk_fp8_f32 v229, v58, v62 op_sel:[0,0,1]
	v_add_u32_e32 v238, 0x3800, v224
	global_store_dwordx4 v238, v[226:229], s[38:39] nt
	v_cvt_pk_fp8_f32 v230, v3, v7
	v_cvt_pk_fp8_f32 v231, v19, v23
	v_cvt_pk_fp8_f32 v232, v35, v39
	v_cvt_pk_fp8_f32 v233, v51, v55
	v_cvt_pk_fp8_f32 v230, v11, v15 op_sel:[0,0,1]
	v_cvt_pk_fp8_f32 v231, v27, v31 op_sel:[0,0,1]
	v_cvt_pk_fp8_f32 v232, v43, v47 op_sel:[0,0,1]
	v_cvt_pk_fp8_f32 v233, v59, v63 op_sel:[0,0,1]
	v_add_u32_e32 v238, 0x5400, v224
	global_store_dwordx4 v238, v[230:233], s[38:39] nt
	s_mov_b32 s27, 1
	s_mov_b32 s30, 7
; __device__ __forceinline__ bool titem_group(int& it, TItem& t, const float* W, size_t wstride, int nmat, int K, int N, const float* gain, float scale, void* WT, size_t tstride_bytes, int mode, int fp8) {
;     const int nblk = N / 64, per = (K / 64) * nblk, tot = per * nmat;
;     if (it >= tot) { it -= tot; return false; }
;     const int mat = it / per, r = it % per, k0 = 64 * (r / nblk), n0 = 64 * (r % nblk), esz = (fp8 == 1) ? 1 : 2;
;     const int drow0 = (mode == 0) ? n0 : (256 * (n0 / 128) + (n0 % 128) + (mode == 2 ? 128 : 0));
;     t.src = W + (size_t)mat * wstride + (size_t)k0 * N + n0; t.gain = gain ? gain + k0 : nullptr;
;     t.dst = (unsigned char*)WT + (size_t)mat * tstride_bytes + ((size_t)drow0 * K + k0) * esz; t.ldw = N; t.ldwt = K * esz; t.fp8 = fp8; t.scale = scale; return true;
; }
; __device__ __forceinline__ void titem_load(const TItem& t, f32x4 (&v)[2][8], f32x4 (&g)[2], int lane) {
;     const int n4 = lane & 7, kr = lane >> 3;
;     const float* gp = t.gain ? t.gain : t.src;
; #pragma unroll
;     for (int h = 0; h < 2; ++h)
; #pragma unroll
;         for (int i = 0; i < 8; ++i) v[h][i] = *(const f32x4*)(t.src + (size_t)(8 * kr + i) * t.ldw + 32 * h + 4 * n4);
;     g[0] = *(const f32x4*)(gp + 8 * kr); g[1] = *(const f32x4*)(gp + 8 * kr + 4);
; }
; __device__ __forceinline__ void titem_process(const TItem& t, const f32x4 (&v)[2][8], const f32x4 (&g)[2], int lane) {
;     const int n4 = lane & 7, kr = lane >> 3;
;     float s[8];
; #pragma unroll
;     for (int j = 0; j < 8; ++j) s[j] = t.gain ? g[j >> 2][j & 3] * t.scale : t.scale;
;     if (t.fp8 == 1) {
; #pragma unroll
;         for (int h = 0; h < 2; ++h)
; #pragma unroll
;             for (int i = 0; i < 4; ++i) { u32x2 o; o.x = epi::pk4_fp8(v[h][0][i] * s[0], v[h][1][i] * s[1], v[h][2][i] * s[2], v[h][3][i] * s[3]); o.y = epi::pk4_fp8(v[h][4][i] * s[4], v[h][5][i] * s[5], v[h][6][i] * s[6], v[h][7][i] * s[7]);
;                 __builtin_nontemporal_store(o, (u32x2*)(t.dst + (size_t)(32 * h + 4 * n4 + i) * t.ldwt + 8 * kr)); }
.Lcv1_dn:
	s_add_i32 s35, s27, 1
	s_min_u32 s35, s35, 13
	s_lshl_b32 s37, s35, 11
	s_add_i32 s37, s37, s25
	s_lshr_b32 s45, s37, 9
	s_mul_i32 s45, s45, 0x2493
	s_lshr_b32 s45, s45, 16
	s_mul_i32 s51, s45, 0xe00
	s_sub_i32 s50, s37, s51
	s_lshr_b32 s51, s50, 6
	s_and_b32 s52, s50, 63
	s_mul_i32 s63, s45, 0x3800000
	s_add_u32 s46, s4, s63
	s_addc_u32 s47, s5, 0
	s_lshl_b32 s63, s51, 20
	s_lshl_b32 s37, s52, 7
	s_add_i32 s63, s63, s37
	s_add_u32 s46, s46, s63
	s_addc_u32 s47, s47, 0
	s_mov_b64 s[48:49], s[4:5]
	s_mul_i32 s63, s45, 0xe00000
	s_mul_i32 s37, s52, 0x38000
	s_add_i32 s63, s63, s37
	s_lshl_b32 s37, s51, 7
	s_add_i32 s63, s63, s37
	s_add_u32 s38, s8, s63
	s_addc_u32 s39, s9, 0
	global_load_dwordx4 v[0:3], v221, s[46:47]
	v_add_u32_e32 v238, 0x2000, v221
	global_load_dwordx4 v[4:7], v238, s[46:47]
	v_add_u32_e32 v238, 0x4000, v221
	global_load_dwordx4 v[8:11], v238, s[46:47]
	v_add_u32_e32 v238, 0x6000, v221
	global_load_dwordx4 v[12:15], v238, s[46:47]
	v_add_u32_e32 v238, 0x8000, v221
	global_load_dwordx4 v[16:19], v238, s[46:47]
	v_add_u32_e32 v238, 0xa000, v221
	global_load_dwordx4 v[20:23], v238, s[46:47]
	v_add_u32_e32 v238, 0xc000, v221
	global_load_dwordx4 v[24:27], v238, s[46:47]
	v_add_u32_e32 v238, 0xe000, v221
	global_load_dwordx4 v[28:31], v238, s[46:47]
	v_add_u32_e32 v238, 0x10000, v221
	global_load_dwordx4 v[32:35], v238, s[46:47]
	v_add_u32_e32 v238, 0x12000, v221
	global_load_dwordx4 v[36:39], v238, s[46:47]
	v_add_u32_e32 v238, 0x14000, v221
	global_load_dwordx4 v[40:43], v238, s[46:47]
	v_add_u32_e32 v238, 0x16000, v221
	global_load_dwordx4 v[44:47], v238, s[46:47]
	v_add_u32_e32 v238, 0x18000, v221
	global_load_dwordx4 v[48:51], v238, s[46:47]
	v_add_u32_e32 v238, 0x1a000, v221
	global_load_dwordx4 v[52:55], v238, s[46:47]
	v_add_u32_e32 v238, 0x1c000, v221
	global_load_dwordx4 v[56:59], v238, s[46:47]
	v_add_u32_e32 v238, 0x1e000, v221
	global_load_dwordx4 v[60:63], v238, s[46:47]
	global_load_dwordx4 v[128:131], v222, s[48:49]
	global_load_dwordx4 v[132:135], v222, s[48:49] offset:16
	global_load_dwordx4 v[136:139], v222, s[48:49] offset:32
	global_load_dwordx4 v[140:143], v222, s[48:49] offset:48
	s_waitcnt vmcnt(24)
	v_mov_b32_e32 v160, 0x44000000
	v_mov_b32_e32 v161, 0x44000000
	v_mov_b32_e32 v162, 0x44000000
	v_mov_b32_e32 v163, 0x44000000
	v_mov_b32_e32 v164, 0x44000000
	v_mov_b32_e32 v165, 0x44000000
	v_mov_b32_e32 v166, 0x44000000
	v_mov_b32_e32 v167, 0x44000000
	v_mov_b32_e32 v168, 0x44000000
	v_mov_b32_e32 v169, 0x44000000
	v_mov_b32_e32 v170, 0x44000000
	v_mov_b32_e32 v171, 0x44000000
	v_mov_b32_e32 v172, 0x44000000
	v_mov_b32_e32 v173, 0x44000000
	v_mov_b32_e32 v174, 0x44000000
	v_mov_b32_e32 v175, 0x44000000
	v_pk_mul_f32 v[64:65], v[64:65], v[160:161] op_sel:[0,0] op_sel_hi:[1,0]
	v_pk_mul_f32 v[66:67], v[66:67], v[160:161] op_sel:[0,0] op_sel_hi:[1,0]
	v_pk_mul_f32 v[68:69], v[68:69], v[160:161] op_sel:[0,1] op_sel_hi:[1,1]
	v_pk_mul_f32 v[70:71], v[70:71], v[160:161] op_sel:[0,1] op_sel_hi:[1,1]
	v_pk_mul_f32 v[72:73], v[72:73], v[162:163] op_sel:[0,0] op_sel_hi:[1,0]
	v_pk_mul_f32 v[74:75], v[74:75], v[162:163] op_sel:[0,0] op_sel_hi:[1,0]
	v_pk_mul_f32 v[76:77], v[76:77], v[162:163] op_sel:[0,1] op_sel_hi:[1,1]
	v_pk_mul_f32 v[78:79], v[78:79], v[162:163] op_sel:[0,1] op_sel_hi:[1,1]
	v_pk_mul_f32 v[80:81], v[80:81], v[164:165] op_sel:[0,0] op_sel_hi:[1,0]
	v_pk_mul_f32 v[82:83], v[82:83], v[164:165] op_sel:[0,0] op_sel_hi:[1,0]
	v_pk_mul_f32 v[84:85], v[84:85], v[164:165] op_sel:[0,1] op_sel_hi:[1,1]
	v_pk_mul_f32 v[86:87], v[86:87], v[164:165] op_sel:[0,1] op_sel_hi:[1,1]
	v_pk_mul_f32 v[88:89], v[88:89], v[166:167] op_sel:[0,0] op_sel_hi:[1,0]
	v_pk_mul_f32 v[90:91], v[90:91], v[166:167] op_sel:[0,0] op_sel_hi:[1,0]
	v_pk_mul_f32 v[92:93], v[92:93], v[166:167] op_sel:[0,1] op_sel_hi:[1,1]
	v_pk_mul_f32 v[94:95], v[94:95], v[166:167] op_sel:[0,1] op_sel_hi:[1,1]
	v_pk_mul_f32 v[96:97], v[96:97], v[168:169] op_sel:[0,0] op_sel_hi:[1,0]
	v_pk_mul_f32 v[98:99], v[98:99], v[168:169] op_sel:[0,0] op_sel_hi:[1,0]
	v_pk_mul_f32 v[100:101], v[100:101], v[168:169] op_sel:[0,1] op_sel_hi:[1,1]
	v_pk_mul_f32 v[102:103], v[102:103], v[168:169] op_sel:[0,1] op_sel_hi:[1,1]
	v_pk_mul_f32 v[104:105], v[104:105], v[170:171] op_sel:[0,0] op_sel_hi:[1,0]
	v_pk_mul_f32 v[106:107], v[106:107], v[170:171] op_sel:[0,0] op_sel_hi:[1,0]
	v_pk_mul_f32 v[108:109], v[108:109], v[170:171] op_sel:[0,1] op_sel_hi:[1,1]
	v_pk_mul_f32 v[110:111], v[110:111], v[170:171] op_sel:[0,1] op_sel_hi:[1,1]
	v_pk_mul_f32 v[112:113], v[112:113], v[172:173] op_sel:[0,0] op_sel_hi:[1,0]
	v_pk_mul_f32 v[114:115], v[114:115], v[172:173] op_sel:[0,0] op_sel_hi:[1,0]
	v_pk_mul_f32 v[116:117], v[116:117], v[172:173] op_sel:[0,1] op_sel_hi:[1,1]
	v_pk_mul_f32 v[118:119], v[118:119], v[172:173] op_sel:[0,1] op_sel_hi:[1,1]
	v_pk_mul_f32 v[120:121], v[120:121], v[174:175] op_sel:[0,0] op_sel_hi:[1,0]
	v_pk_mul_f32 v[122:123], v[122:123], v[174:175] op_sel:[0,0] op_sel_hi:[1,0]
	v_pk_mul_f32 v[124:125], v[124:125], v[174:175] op_sel:[0,1] op_sel_hi:[1,1]
	v_pk_mul_f32 v[126:127], v[126:127], v[174:175] op_sel:[0,1] op_sel_hi:[1,1]
	v_med3_f32 v64, v64, s33, v225
	v_med3_f32 v65, v65, s33, v225
	v_med3_f32 v66, v66, s33, v225
	v_med3_f32 v67, v67, s33, v225
	v_med3_f32 v68, v68, s33, v225
	v_med3_f32 v69, v69, s33, v225
	v_med3_f32 v70, v70, s33, v225
	v_med3_f32 v71, v71, s33, v225
	v_med3_f32 v72, v72, s33, v225
	v_med3_f32 v73, v73, s33, v225
	v_med3_f32 v74, v74, s33, v225
	v_med3_f32 v75, v75, s33, v225
	v_med3_f32 v76, v76, s33, v225
	v_med3_f32 v77, v77, s33, v225
	v_med3_f32 v78, v78, s33, v225
	v_med3_f32 v79, v79, s33, v225
; __device__ __forceinline__ bool titem_group(int& it, TItem& t, const float* W, size_t wstride, int nmat, int K, int N, const float* gain, float scale, void* WT, size_t tstride_bytes, int mode, int fp8) {
;     const int nblk = N / 64, per = (K / 64) * nblk, tot = per * nmat;
;     if (it >= tot) { it -= tot; return false; }
;     const int mat = it / per, r = it % per, k0 = 64 * (r / nblk), n0 = 64 * (r % nblk), esz = (fp8 == 1) ? 1 : 2;
;     const int drow0 = (mode == 0) ? n0 : (256 * (n0 / 128) + (n0 % 128) + (mode == 2 ? 128 : 0));
;     t.src = W + (size_t)mat * wstride + (size_t)k0 * N + n0; t.gain = gain ? gain + k0 : nullptr;
;     t.dst = (unsigned char*)WT + (size_t)mat * tstride_bytes + ((size_t)drow0 * K + k0) * esz; t.ldw = N; t.ldwt = K * esz; t.fp8 = fp8; t.scale = scale; return true;
; }
; __device__ __forceinline__ void titem_load(const TItem& t, f32x4 (&v)[2][8], f32x4 (&g)[2], int lane) {
;     const int n4 = lane & 7, kr = lane >> 3;
;     const float* gp = t.gain ? t.gain : t.src;
; #pragma unroll
;     for (int h = 0; h < 2; ++h)
; #pragma unroll
;         for (int i = 0; i < 8; ++i) v[h][i] = *(const f32x4*)(t.src + (size_t)(8 * kr + i) * t.ldw + 32 * h + 4 * n4);
;     g[0] = *(const f32x4*)(gp + 8 * kr); g[1] = *(const f32x4*)(gp + 8 * kr + 4);
; }
; __device__ __forceinline__ void titem_process(const TItem& t, const f32x4 (&v)[2][8], const f32x4 (&g)[2], int lane) {
;     const int n4 = lane & 7, kr = lane >> 3;
;     float s[8];
; #pragma unroll
;     for (int j = 0; j < 8; ++j) s[j] = t.gain ? g[j >> 2][j & 3] * t.scale : t.scale;
;     if (t.fp8 == 1) {
; #pragma unroll
;         for (int h = 0; h < 2; ++h)
; #pragma unroll
;             for (int i = 0; i < 4; ++i) { u32x2 o; o.x = epi::pk4_fp8(v[h][0][i] * s[0], v[h][1][i] * s[1], v[h][2][i] * s[2], v[h][3][i] * s[3]); o.y = epi::pk4_fp8(v[h][4][i] * s[4], v[h][5][i] * s[5], v[h][6][i] * s[6], v[h][7][i] * s[7]);
;                 __builtin_nontemporal_store(o, (u32x2*)(t.dst + (size_t)(32 * h + 4 * n4 + i) * t.ldwt + 8 * kr)); }
	v_med3_f32 v80, v80, s33, v225
	v_med3_f32 v81, v81, s33, v225
	v_med3_f32 v82, v82, s33, v225
	v_med3_f32 v83, v83, s33, v225
	v_med3_f32 v84, v84, s33, v225
	v_med3_f32 v85, v85, s33, v225
	v_med3_f32 v86, v86, s33, v225
	v_med3_f32 v87, v87, s33, v225
	v_med3_f32 v88, v88, s33, v225
	v_med3_f32 v89, v89, s33, v225
	v_med3_f32 v90, v90, s33, v225
	v_med3_f32 v91, v91, s33, v225
	v_med3_f32 v92, v92, s33, v225
	v_med3_f32 v93, v93, s33, v225
	v_med3_f32 v94, v94, s33, v225
	v_med3_f32 v95, v95, s33, v225
	v_med3_f32 v96, v96, s33, v225
	v_med3_f32 v97, v97, s33, v225
	v_med3_f32 v98, v98, s33, v225
	v_med3_f32 v99, v99, s33, v225
	v_med3_f32 v100, v100, s33, v225
	v_med3_f32 v101, v101, s33, v225
	v_med3_f32 v102, v102, s33, v225
	v_med3_f32 v103, v103, s33, v225
	v_med3_f32 v104, v104, s33, v225
	v_med3_f32 v105, v105, s33, v225
	v_med3_f32 v106, v106, s33, v225
	v_med3_f32 v107, v107, s33, v225
	v_med3_f32 v108, v108, s33, v225
	v_med3_f32 v109, v109, s33, v225
	v_med3_f32 v110, v110, s33, v225
	v_med3_f32 v111, v111, s33, v225
	v_med3_f32 v112, v112, s33, v225
	v_med3_f32 v113, v113, s33, v225
	v_med3_f32 v114, v114, s33, v225
	v_med3_f32 v115, v115, s33, v225
	v_med3_f32 v116, v116, s33, v225
	v_med3_f32 v117, v117, s33, v225
	v_med3_f32 v118, v118, s33, v225
	v_med3_f32 v119, v119, s33, v225
	v_med3_f32 v120, v120, s33, v225
	v_med3_f32 v121, v121, s33, v225
	v_med3_f32 v122, v122, s33, v225
	v_med3_f32 v123, v123, s33, v225
	v_med3_f32 v124, v124, s33, v225
	v_med3_f32 v125, v125, s33, v225
	v_med3_f32 v126, v126, s33, v225
	v_med3_f32 v127, v127, s33, v225
	v_cvt_pk_fp8_f32 v226, v64, v68
	v_cvt_pk_fp8_f32 v227, v80, v84
	v_cvt_pk_fp8_f32 v228, v96, v100
	v_cvt_pk_fp8_f32 v229, v112, v116
	v_cvt_pk_fp8_f32 v226, v72, v76 op_sel:[0,0,1]
	v_cvt_pk_fp8_f32 v227, v88, v92 op_sel:[0,0,1]
	v_cvt_pk_fp8_f32 v228, v104, v108 op_sel:[0,0,1]
	v_cvt_pk_fp8_f32 v229, v120, v124 op_sel:[0,0,1]
	s_nop 0
	global_store_dwordx4 v224, v[226:229], s[40:41] nt
	v_cvt_pk_fp8_f32 v230, v65, v69
	v_cvt_pk_fp8_f32 v231, v81, v85
	v_cvt_pk_fp8_f32 v232, v97, v101
	v_cvt_pk_fp8_f32 v233, v113, v117
	v_cvt_pk_fp8_f32 v230, v73, v77 op_sel:[0,0,1]
	v_cvt_pk_fp8_f32 v231, v89, v93 op_sel:[0,0,1]
	v_cvt_pk_fp8_f32 v232, v105, v109 op_sel:[0,0,1]
	v_cvt_pk_fp8_f32 v233, v121, v125 op_sel:[0,0,1]
	v_add_u32_e32 v238, 0x1c00, v224
	global_store_dwordx4 v238, v[230:233], s[40:41] nt
	v_cvt_pk_fp8_f32 v226, v66, v70
	v_cvt_pk_fp8_f32 v227, v82, v86
	v_cvt_pk_fp8_f32 v228, v98, v102
	v_cvt_pk_fp8_f32 v229, v114, v118
	v_cvt_pk_fp8_f32 v226, v74, v78 op_sel:[0,0,1]
	v_cvt_pk_fp8_f32 v227, v90, v94 op_sel:[0,0,1]
	v_cvt_pk_fp8_f32 v228, v106, v110 op_sel:[0,0,1]
	v_cvt_pk_fp8_f32 v229, v122, v126 op_sel:[0,0,1]
	v_add_u32_e32 v238, 0x3800, v224
	global_store_dwordx4 v238, v[226:229], s[40:41] nt
	v_cvt_pk_fp8_f32 v230, v67, v71
	v_cvt_pk_fp8_f32 v231, v83, v87
	v_cvt_pk_fp8_f32 v232, v99, v103
	v_cvt_pk_fp8_f32 v233, v115, v119
	v_cvt_pk_fp8_f32 v230, v75, v79 op_sel:[0,0,1]
	v_cvt_pk_fp8_f32 v231, v91, v95 op_sel:[0,0,1]
	v_cvt_pk_fp8_f32 v232, v107, v111 op_sel:[0,0,1]
	v_cvt_pk_fp8_f32 v233, v123, v127 op_sel:[0,0,1]
	v_add_u32_e32 v238, 0x5400, v224
	global_store_dwordx4 v238, v[230:233], s[40:41] nt
	s_add_i32 s35, s27, 2
	s_min_u32 s35, s35, 13
	s_lshl_b32 s37, s35, 11
	s_add_i32 s37, s37, s25
	s_lshr_b32 s45, s37, 9
	s_mul_i32 s45, s45, 0x2493
	s_lshr_b32 s45, s45, 16
	s_mul_i32 s51, s45, 0xe00
	s_sub_i32 s50, s37, s51
	s_lshr_b32 s51, s50, 6
	s_and_b32 s52, s50, 63
	s_mul_i32 s63, s45, 0x3800000
	s_add_u32 s46, s4, s63
	s_addc_u32 s47, s5, 0
	s_lshl_b32 s63, s51, 20
	s_lshl_b32 s37, s52, 7
	s_add_i32 s63, s63, s37
	s_add_u32 s46, s46, s63
	s_addc_u32 s47, s47, 0
	s_mov_b64 s[48:49], s[4:5]
	s_mul_i32 s63, s45, 0xe00000
	s_mul_i32 s37, s52, 0x38000
	s_add_i32 s63, s63, s37
	s_lshl_b32 s37, s51, 7
	s_add_i32 s63, s63, s37
	s_add_u32 s40, s8, s63
	s_addc_u32 s41, s9, 0
	global_load_dwordx4 v[64:67], v221, s[46:47]
	v_add_u32_e32 v238, 0x2000, v221
	global_load_dwordx4 v[68:71], v238, s[46:47]
	v_add_u32_e32 v238, 0x4000, v221
	global_load_dwordx4 v[72:75], v238, s[46:47]
	v_add_u32_e32 v238, 0x6000, v221
	global_load_dwordx4 v[76:79], v238, s[46:47]
	v_add_u32_e32 v238, 0x8000, v221
	global_load_dwordx4 v[80:83], v238, s[46:47]
	v_add_u32_e32 v238, 0xa000, v221
	global_load_dwordx4 v[84:87], v238, s[46:47]
	v_add_u32_e32 v238, 0xc000, v221
	global_load_dwordx4 v[88:91], v238, s[46:47]
	v_add_u32_e32 v238, 0xe000, v221
	global_load_dwordx4 v[92:95], v238, s[46:47]
	v_add_u32_e32 v238, 0x10000, v221
	global_load_dwordx4 v[96:99], v238, s[46:47]
	v_add_u32_e32 v238, 0x12000, v221
	global_load_dwordx4 v[100:103], v238, s[46:47]
	v_add_u32_e32 v238, 0x14000, v221
	global_load_dwordx4 v[104:107], v238, s[46:47]
	v_add_u32_e32 v238, 0x16000, v221
	global_load_dwordx4 v[108:111], v238, s[46:47]
	v_add_u32_e32 v238, 0x18000, v221
	global_load_dwordx4 v[112:115], v238, s[46:47]
	v_add_u32_e32 v238, 0x1a000, v221
	global_load_dwordx4 v[116:119], v238, s[46:47]
	v_add_u32_e32 v238, 0x1c000, v221
	global_load_dwordx4 v[120:123], v238, s[46:47]
	v_add_u32_e32 v238, 0x1e000, v221
	global_load_dwordx4 v[124:127], v238, s[46:47]
	global_load_dwordx4 v[144:147], v222, s[48:49]
	global_load_dwordx4 v[148:151], v222, s[48:49] offset:16
	global_load_dwordx4 v[152:155], v222, s[48:49] offset:32
	global_load_dwordx4 v[156:159], v222, s[48:49] offset:48
	s_waitcnt vmcnt(24)
; __device__ __forceinline__ void titem_process(const TItem& t, const f32x4 (&v)[2][8], const f32x4 (&g)[2], int lane) {
;     const int n4 = lane & 7, kr = lane >> 3;
;     float s[8];
; #pragma unroll
;     for (int j = 0; j < 8; ++j) s[j] = t.gain ? g[j >> 2][j & 3] * t.scale : t.scale;
;     if (t.fp8 == 1) {
; #pragma unroll
;         for (int h = 0; h < 2; ++h)
; #pragma unroll
;             for (int i = 0; i < 4; ++i) { u32x2 o; o.x = epi::pk4_fp8(v[h][0][i] * s[0], v[h][1][i] * s[1], v[h][2][i] * s[2], v[h][3][i] * s[3]); o.y = epi::pk4_fp8(v[h][4][i] * s[4], v[h][5][i] * s[5], v[h][6][i] * s[6], v[h][7][i] * s[7]);
;                 __builtin_nontemporal_store(o, (u32x2*)(t.dst + (size_t)(32 * h + 4 * n4 + i) * t.ldwt + 8 * kr)); }
	v_mov_b32_e32 v160, 0x44000000
	v_mov_b32_e32 v161, 0x44000000
	v_mov_b32_e32 v162, 0x44000000
	v_mov_b32_e32 v163, 0x44000000
	v_mov_b32_e32 v164, 0x44000000
	v_mov_b32_e32 v165, 0x44000000
	v_mov_b32_e32 v166, 0x44000000
	v_mov_b32_e32 v167, 0x44000000
	v_mov_b32_e32 v168, 0x44000000
	v_mov_b32_e32 v169, 0x44000000
	v_mov_b32_e32 v170, 0x44000000
	v_mov_b32_e32 v171, 0x44000000
	v_mov_b32_e32 v172, 0x44000000
	v_mov_b32_e32 v173, 0x44000000
	v_mov_b32_e32 v174, 0x44000000
	v_mov_b32_e32 v175, 0x44000000
	v_pk_mul_f32 v[0:1], v[0:1], v[160:161] op_sel:[0,0] op_sel_hi:[1,0]
	v_pk_mul_f32 v[2:3], v[2:3], v[160:161] op_sel:[0,0] op_sel_hi:[1,0]
	v_pk_mul_f32 v[4:5], v[4:5], v[160:161] op_sel:[0,1] op_sel_hi:[1,1]
	v_pk_mul_f32 v[6:7], v[6:7], v[160:161] op_sel:[0,1] op_sel_hi:[1,1]
	v_pk_mul_f32 v[8:9], v[8:9], v[162:163] op_sel:[0,0] op_sel_hi:[1,0]
	v_pk_mul_f32 v[10:11], v[10:11], v[162:163] op_sel:[0,0] op_sel_hi:[1,0]
	v_pk_mul_f32 v[12:13], v[12:13], v[162:163] op_sel:[0,1] op_sel_hi:[1,1]
	v_pk_mul_f32 v[14:15], v[14:15], v[162:163] op_sel:[0,1] op_sel_hi:[1,1]
	v_pk_mul_f32 v[16:17], v[16:17], v[164:165] op_sel:[0,0] op_sel_hi:[1,0]
	v_pk_mul_f32 v[18:19], v[18:19], v[164:165] op_sel:[0,0] op_sel_hi:[1,0]
	v_pk_mul_f32 v[20:21], v[20:21], v[164:165] op_sel:[0,1] op_sel_hi:[1,1]
	v_pk_mul_f32 v[22:23], v[22:23], v[164:165] op_sel:[0,1] op_sel_hi:[1,1]
	v_pk_mul_f32 v[24:25], v[24:25], v[166:167] op_sel:[0,0] op_sel_hi:[1,0]
	v_pk_mul_f32 v[26:27], v[26:27], v[166:167] op_sel:[0,0] op_sel_hi:[1,0]
	v_pk_mul_f32 v[28:29], v[28:29], v[166:167] op_sel:[0,1] op_sel_hi:[1,1]
	v_pk_mul_f32 v[30:31], v[30:31], v[166:167] op_sel:[0,1] op_sel_hi:[1,1]
	v_pk_mul_f32 v[32:33], v[32:33], v[168:169] op_sel:[0,0] op_sel_hi:[1,0]
	v_pk_mul_f32 v[34:35], v[34:35], v[168:169] op_sel:[0,0] op_sel_hi:[1,0]
	v_pk_mul_f32 v[36:37], v[36:37], v[168:169] op_sel:[0,1] op_sel_hi:[1,1]
	v_pk_mul_f32 v[38:39], v[38:39], v[168:169] op_sel:[0,1] op_sel_hi:[1,1]
	v_pk_mul_f32 v[40:41], v[40:41], v[170:171] op_sel:[0,0] op_sel_hi:[1,0]
	v_pk_mul_f32 v[42:43], v[42:43], v[170:171] op_sel:[0,0] op_sel_hi:[1,0]
	v_pk_mul_f32 v[44:45], v[44:45], v[170:171] op_sel:[0,1] op_sel_hi:[1,1]
	v_pk_mul_f32 v[46:47], v[46:47], v[170:171] op_sel:[0,1] op_sel_hi:[1,1]
	v_pk_mul_f32 v[48:49], v[48:49], v[172:173] op_sel:[0,0] op_sel_hi:[1,0]
	v_pk_mul_f32 v[50:51], v[50:51], v[172:173] op_sel:[0,0] op_sel_hi:[1,0]
	v_pk_mul_f32 v[52:53], v[52:53], v[172:173] op_sel:[0,1] op_sel_hi:[1,1]
	v_pk_mul_f32 v[54:55], v[54:55], v[172:173] op_sel:[0,1] op_sel_hi:[1,1]
	v_pk_mul_f32 v[56:57], v[56:57], v[174:175] op_sel:[0,0] op_sel_hi:[1,0]
	v_pk_mul_f32 v[58:59], v[58:59], v[174:175] op_sel:[0,0] op_sel_hi:[1,0]
	v_pk_mul_f32 v[60:61], v[60:61], v[174:175] op_sel:[0,1] op_sel_hi:[1,1]
	v_pk_mul_f32 v[62:63], v[62:63], v[174:175] op_sel:[0,1] op_sel_hi:[1,1]
	v_med3_f32 v0, v0, s33, v225
	v_med3_f32 v1, v1, s33, v225
	v_med3_f32 v2, v2, s33, v225
	v_med3_f32 v3, v3, s33, v225
	v_med3_f32 v4, v4, s33, v225
	v_med3_f32 v5, v5, s33, v225
	v_med3_f32 v6, v6, s33, v225
	v_med3_f32 v7, v7, s33, v225
	v_med3_f32 v8, v8, s33, v225
	v_med3_f32 v9, v9, s33, v225
	v_med3_f32 v10, v10, s33, v225
	v_med3_f32 v11, v11, s33, v225
	v_med3_f32 v12, v12, s33, v225
	v_med3_f32 v13, v13, s33, v225
	v_med3_f32 v14, v14, s33, v225
	v_med3_f32 v15, v15, s33, v225
	v_med3_f32 v16, v16, s33, v225
	v_med3_f32 v17, v17, s33, v225
	v_med3_f32 v18, v18, s33, v225
	v_med3_f32 v19, v19, s33, v225
	v_med3_f32 v20, v20, s33, v225
	v_med3_f32 v21, v21, s33, v225
	v_med3_f32 v22, v22, s33, v225
	v_med3_f32 v23, v23, s33, v225
	v_med3_f32 v24, v24, s33, v225
	v_med3_f32 v25, v25, s33, v225
	v_med3_f32 v26, v26, s33, v225
	v_med3_f32 v27, v27, s33, v225
	v_med3_f32 v28, v28, s33, v225
	v_med3_f32 v29, v29, s33, v225
	v_med3_f32 v30, v30, s33, v225
	v_med3_f32 v31, v31, s33, v225
	v_med3_f32 v32, v32, s33, v225
	v_med3_f32 v33, v33, s33, v225
	v_med3_f32 v34, v34, s33, v225
	v_med3_f32 v35, v35, s33, v225
	v_med3_f32 v36, v36, s33, v225
	v_med3_f32 v37, v37, s33, v225
	v_med3_f32 v38, v38, s33, v225
	v_med3_f32 v39, v39, s33, v225
	v_med3_f32 v40, v40, s33, v225
	v_med3_f32 v41, v41, s33, v225
	v_med3_f32 v42, v42, s33, v225
	v_med3_f32 v43, v43, s33, v225
	v_med3_f32 v44, v44, s33, v225
	v_med3_f32 v45, v45, s33, v225
	v_med3_f32 v46, v46, s33, v225
	v_med3_f32 v47, v47, s33, v225
	v_med3_f32 v48, v48, s33, v225
	v_med3_f32 v49, v49, s33, v225
	v_med3_f32 v50, v50, s33, v225
	v_med3_f32 v51, v51, s33, v225
	v_med3_f32 v52, v52, s33, v225
	v_med3_f32 v53, v53, s33, v225
	v_med3_f32 v54, v54, s33, v225
	v_med3_f32 v55, v55, s33, v225
	v_med3_f32 v56, v56, s33, v225
	v_med3_f32 v57, v57, s33, v225
	v_med3_f32 v58, v58, s33, v225
	v_med3_f32 v59, v59, s33, v225
	v_med3_f32 v60, v60, s33, v225
	v_med3_f32 v61, v61, s33, v225
	v_med3_f32 v62, v62, s33, v225
	v_med3_f32 v63, v63, s33, v225
	v_cvt_pk_fp8_f32 v226, v0, v4
	v_cvt_pk_fp8_f32 v227, v16, v20
	v_cvt_pk_fp8_f32 v228, v32, v36
	v_cvt_pk_fp8_f32 v229, v48, v52
	v_cvt_pk_fp8_f32 v226, v8, v12 op_sel:[0,0,1]
	v_cvt_pk_fp8_f32 v227, v24, v28 op_sel:[0,0,1]
	v_cvt_pk_fp8_f32 v228, v40, v44 op_sel:[0,0,1]
	v_cvt_pk_fp8_f32 v229, v56, v60 op_sel:[0,0,1]
	s_nop 0
	global_store_dwordx4 v224, v[226:229], s[38:39] nt
	v_cvt_pk_fp8_f32 v230, v1, v5
	v_cvt_pk_fp8_f32 v231, v17, v21
	v_cvt_pk_fp8_f32 v232, v33, v37
	v_cvt_pk_fp8_f32 v233, v49, v53
	v_cvt_pk_fp8_f32 v230, v9, v13 op_sel:[0,0,1]
	v_cvt_pk_fp8_f32 v231, v25, v29 op_sel:[0,0,1]
	v_cvt_pk_fp8_f32 v232, v41, v45 op_sel:[0,0,1]
	v_cvt_pk_fp8_f32 v233, v57, v61 op_sel:[0,0,1]
	v_add_u32_e32 v238, 0x1c00, v224
	global_store_dwordx4 v238, v[230:233], s[38:39] nt
	v_cvt_pk_fp8_f32 v226, v2, v6
	v_cvt_pk_fp8_f32 v227, v18, v22
	v_cvt_pk_fp8_f32 v228, v34, v38
	v_cvt_pk_fp8_f32 v229, v50, v54
	v_cvt_pk_fp8_f32 v226, v10, v14 op_sel:[0,0,1]
	v_cvt_pk_fp8_f32 v227, v26, v30 op_sel:[0,0,1]
	v_cvt_pk_fp8_f32 v228, v42, v46 op_sel:[0,0,1]
	v_cvt_pk_fp8_f32 v229, v58, v62 op_sel:[0,0,1]
	v_add_u32_e32 v238, 0x3800, v224
	global_store_dwordx4 v238, v[226:229], s[38:39] nt
	v_cvt_pk_fp8_f32 v230, v3, v7
	v_cvt_pk_fp8_f32 v231, v19, v23
	v_cvt_pk_fp8_f32 v232, v35, v39
	v_cvt_pk_fp8_f32 v233, v51, v55
	v_cvt_pk_fp8_f32 v230, v11, v15 op_sel:[0,0,1]
	v_cvt_pk_fp8_f32 v231, v27, v31 op_sel:[0,0,1]
	v_cvt_pk_fp8_f32 v232, v43, v47 op_sel:[0,0,1]
	v_cvt_pk_fp8_f32 v233, v59, v63 op_sel:[0,0,1]
	v_add_u32_e32 v238, 0x5400, v224
	global_store_dwordx4 v238, v[230:233], s[38:39] nt
	s_add_i32 s27, s27, 2
	s_sub_i32 s30, s30, 1
	s_cmp_lg_u32 s30, 0
	s_cbranch_scc1 .Lcv1_dn
	s_waitcnt vmcnt(0)

; __device__ __forceinline__ bool titem_group(int& it, TItem& t, const float* W, size_t wstride, int nmat, int K, int N, const float* gain, float scale, void* WT, size_t tstride_bytes, int mode, int fp8) {
;     const int nblk = N / 64, per = (K / 64) * nblk, tot = per * nmat;
;     if (it >= tot) { it -= tot; return false; }
;     const int mat = it / per, r = it % per, k0 = 64 * (r / nblk), n0 = 64 * (r % nblk), esz = (fp8 == 1) ? 1 : 2;
;     const int drow0 = (mode == 0) ? n0 : (256 * (n0 / 128) + (n0 % 128) + (mode == 2 ? 128 : 0));
;     t.src = W + (size_t)mat * wstride + (size_t)k0 * N + n0; t.gain = gain ? gain + k0 : nullptr;
;     t.dst = (unsigned char*)WT + (size_t)mat * tstride_bytes + ((size_t)drow0 * K + k0) * esz; t.ldw = N; t.ldwt = K * esz; t.fp8 = fp8; t.scale = scale; return true;
; }
; __device__ __forceinline__ void titem_load(const TItem& t, f32x4 (&v)[2][8], f32x4 (&g)[2], int lane) {
;     const int n4 = lane & 7, kr = lane >> 3;
;     const float* gp = t.gain ? t.gain : t.src;
; #pragma unroll
;     for (int h = 0; h < 2; ++h)
; #pragma unroll
;         for (int i = 0; i < 8; ++i) v[h][i] = *(const f32x4*)(t.src + (size_t)(8 * kr + i) * t.ldw + 32 * h + 4 * n4);
;     g[0] = *(const f32x4*)(gp + 8 * kr); g[1] = *(const f32x4*)(gp + 8 * kr + 4);
; }
.LBB0_942:
	v_readlane_b32 s0, v254, 52
	v_readlane_b32 s1, v254, 53
	s_and_b64 vcc, exec, s[0:1]
	s_cbranch_vccz .LBB0_1082
	v_readlane_b32 s0, v254, 54
	v_readlane_b32 s1, v254, 55
	s_and_b64 vcc, exec, s[0:1]
	s_waitcnt vmcnt(0) lgkmcnt(0)
	s_barrier
	s_cbranch_vccnz .LBB0_1082
	s_load_dwordx2 s[2:3], s[66:67], 0xb0
	s_load_dwordx2 s[4:5], s[66:67], 0xc0
	s_load_dwordx2 s[6:7], s[66:67], 0xc8
	s_load_dwordx2 s[8:9], s[66:67], 0xe0
	v_readlane_b32 s25, v254, 12
	v_mbcnt_lo_u32_b32 v239, -1, 0
	v_mbcnt_hi_u32_b32 v239, -1, v239
	v_and_b32_e32 v237, 7, v239
	v_lshrrev_b32_e32 v203, 3, v239
	v_mul_u32_u24_e32 v220, 0x70000, v203
	v_lshl_add_u32 v220, v237, 4, v220
	v_lshlrev_b32_e32 v221, 17, v203
	v_lshl_add_u32 v221, v237, 4, v221
	v_lshlrev_b32_e32 v222, 6, v203
	v_lshlrev_b32_e32 v223, 13, v237
	v_lshl_add_u32 v223, v203, 4, v223
	v_mul_u32_u24_e32 v224, 0x7000, v237
	v_lshl_add_u32 v224, v203, 4, v224
	v_mov_b32_e32 v225, 0x43e00000
	s_mov_b32 s33, 0xc3e00000
	s_waitcnt lgkmcnt(0)
	s_add_u32 s8, s8, 0xb000000
	s_addc_u32 s9, s9, 0
	s_mov_b32 s35, 0
	s_lshl_b32 s37, s35, 11
	s_add_i32 s37, s37, s25
	s_lshr_b32 s45, s37, 9
	s_mul_i32 s45, s45, 0x2493
	s_lshr_b32 s45, s45, 16
	s_mul_i32 s51, s45, 0xe00
	s_sub_i32 s50, s37, s51
	s_lshr_b32 s51, s50, 5
	s_mul_i32 s51, s51, 0x2493
	s_lshr_b32 s51, s51, 16
	s_mul_i32 s53, s51, 0xe0
	s_sub_i32 s52, s50, s53
	s_and_b32 s53, s45, 7
	s_lshr_b32 s60, s45, 3
	s_cmp_lg_u32 s60, 0
	s_cselect_b32 s46, s6, s4
	s_cselect_b32 s47, s7, s5
	s_mul_i32 s63, s53, 0x3800000
	s_add_u32 s46, s46, s63
	s_addc_u32 s47, s47, 0
	s_mul_i32 s63, s51, 0x380000
	s_lshl_b32 s37, s52, 7
	s_add_i32 s63, s63, s37
	s_add_u32 s46, s46, s63
	s_addc_u32 s47, s47, 0
	s_lshl_b32 s63, s51, 9
	s_add_u32 s48, s2, s63
	s_addc_u32 s49, s3, 0
	s_mul_i32 s63, s53, 0x1c00000
	s_lshr_b32 s37, s52, 2
	s_lshl_b32 s37, s37, 19
	s_add_i32 s63, s63, s37
	s_and_b32 s37, s52, 3
	s_lshl_b32 s37, s37, 16
	s_add_i32 s63, s63, s37
	s_lshl_b32 s37, s60, 18
	s_add_i32 s63, s63, s37
	s_lshl_b32 s37, s51, 7
	s_add_i32 s63, s63, s37
	s_add_u32 s38, s8, s63
	s_addc_u32 s39, s9, 0
	global_load_dwordx4 v[0:3], v220, s[46:47]
	v_add_u32_e32 v238, 0x7000, v220
	global_load_dwordx4 v[4:7], v238, s[46:47]
	v_add_u32_e32 v238, 0xe000, v220
	global_load_dwordx4 v[8:11], v238, s[46:47]
	v_add_u32_e32 v238, 0x15000, v220
	global_load_dwordx4 v[12:15], v238, s[46:47]
	v_add_u32_e32 v238, 0x1c000, v220
	global_load_dwordx4 v[16:19], v238, s[46:47]
	v_add_u32_e32 v238, 0x23000, v220
	global_load_dwordx4 v[20:23], v238, s[46:47]
	v_add_u32_e32 v238, 0x2a000, v220
	global_load_dwordx4 v[24:27], v238, s[46:47]
	v_add_u32_e32 v238, 0x31000, v220
	global_load_dwordx4 v[28:31], v238, s[46:47]
	v_add_u32_e32 v238, 0x38000, v220
	global_load_dwordx4 v[32:35], v238, s[46:47]
	v_add_u32_e32 v238, 0x3f000, v220
	global_load_dwordx4 v[36:39], v238, s[46:47]
	v_add_u32_e32 v238, 0x46000, v220
	global_load_dwordx4 v[40:43], v238, s[46:47]
	v_add_u32_e32 v238, 0x4d000, v220
	global_load_dwordx4 v[44:47], v238, s[46:47]
	v_add_u32_e32 v238, 0x54000, v220
	global_load_dwordx4 v[48:51], v238, s[46:47]
	v_add_u32_e32 v238, 0x5b000, v220
	global_load_dwordx4 v[52:55], v238, s[46:47]
	v_add_u32_e32 v238, 0x62000, v220
	global_load_dwordx4 v[56:59], v238, s[46:47]
	v_add_u32_e32 v238, 0x69000, v220
	global_load_dwordx4 v[60:63], v238, s[46:47]
	global_load_dwordx4 v[128:131], v222, s[48:49]
	global_load_dwordx4 v[132:135], v222, s[48:49] offset:16
	global_load_dwordx4 v[136:139], v222, s[48:49] offset:32
	global_load_dwordx4 v[140:143], v222, s[48:49] offset:48
	s_mov_b32 s35, 1
	s_lshl_b32 s37, s35, 11
	s_add_i32 s37, s37, s25
	s_lshr_b32 s45, s37, 9
	s_mul_i32 s45, s45, 0x2493
	s_lshr_b32 s45, s45, 16
	s_mul_i32 s51, s45, 0xe00
	s_sub_i32 s50, s37, s51
	s_lshr_b32 s51, s50, 5
	s_mul_i32 s51, s51, 0x2493
	s_lshr_b32 s51, s51, 16
	s_mul_i32 s53, s51, 0xe0
	s_sub_i32 s52, s50, s53
	s_and_b32 s53, s45, 7
	s_lshr_b32 s60, s45, 3
	s_cmp_lg_u32 s60, 0
	s_cselect_b32 s46, s6, s4
	s_cselect_b32 s47, s7, s5
	s_mul_i32 s63, s53, 0x3800000
	s_add_u32 s46, s46, s63
	s_addc_u32 s47, s47, 0
	s_mul_i32 s63, s51, 0x380000
	s_lshl_b32 s37, s52, 7
	s_add_i32 s63, s63, s37
	s_add_u32 s46, s46, s63
	s_addc_u32 s47, s47, 0
	s_lshl_b32 s63, s51, 9
	s_add_u32 s48, s2, s63
	s_addc_u32 s49, s3, 0
	s_mul_i32 s63, s53, 0x1c00000
	s_lshr_b32 s37, s52, 2
	s_lshl_b32 s37, s37, 19
	s_add_i32 s63, s63, s37
	s_and_b32 s37, s52, 3
	s_lshl_b32 s37, s37, 16
	s_add_i32 s63, s63, s37
	s_lshl_b32 s37, s60, 18
	s_add_i32 s63, s63, s37
	s_lshl_b32 s37, s51, 7
	s_add_i32 s63, s63, s37
	s_add_u32 s40, s8, s63
	s_addc_u32 s41, s9, 0
	global_load_dwordx4 v[64:67], v220, s[46:47]
	v_add_u32_e32 v238, 0x7000, v220
	global_load_dwordx4 v[68:71], v238, s[46:47]
	v_add_u32_e32 v238, 0xe000, v220
	global_load_dwordx4 v[72:75], v238, s[46:47]
	v_add_u32_e32 v238, 0x15000, v220
	global_load_dwordx4 v[76:79], v238, s[46:47]
	v_add_u32_e32 v238, 0x1c000, v220
	global_load_dwordx4 v[80:83], v238, s[46:47]
	v_add_u32_e32 v238, 0x23000, v220
	global_load_dwordx4 v[84:87], v238, s[46:47]
	v_add_u32_e32 v238, 0x2a000, v220
	global_load_dwordx4 v[88:91], v238, s[46:47]
	v_add_u32_e32 v238, 0x31000, v220
	global_load_dwordx4 v[92:95], v238, s[46:47]
	v_add_u32_e32 v238, 0x38000, v220
	global_load_dwordx4 v[96:99], v238, s[46:47]
	v_add_u32_e32 v238, 0x3f000, v220
	global_load_dwordx4 v[100:103], v238, s[46:47]
	v_add_u32_e32 v238, 0x46000, v220
	global_load_dwordx4 v[104:107], v238, s[46:47]
	v_add_u32_e32 v238, 0x4d000, v220
	global_load_dwordx4 v[108:111], v238, s[46:47]
	v_add_u32_e32 v238, 0x54000, v220
	global_load_dwordx4 v[112:115], v238, s[46:47]
	v_add_u32_e32 v238, 0x5b000, v220
	global_load_dwordx4 v[116:119], v238, s[46:47]
	v_add_u32_e32 v238, 0x62000, v220
	global_load_dwordx4 v[120:123], v238, s[46:47]
	v_add_u32_e32 v238, 0x69000, v220
	global_load_dwordx4 v[124:127], v238, s[46:47]
	global_load_dwordx4 v[144:147], v222, s[48:49]
	global_load_dwordx4 v[148:151], v222, s[48:49] offset:16
	global_load_dwordx4 v[152:155], v222, s[48:49] offset:32
	global_load_dwordx4 v[156:159], v222, s[48:49] offset:48
	s_waitcnt vmcnt(20)
; __device__ __forceinline__ void titem_process(const TItem& t, const f32x4 (&v)[2][8], const f32x4 (&g)[2], int lane) {
;     const int n4 = lane & 7, kr = lane >> 3;
;     float s[8];
; #pragma unroll
;     for (int j = 0; j < 8; ++j) s[j] = t.gain ? g[j >> 2][j & 3] * t.scale : t.scale;
;     if (t.fp8 == 1) {
; #pragma unroll
;         for (int h = 0; h < 2; ++h)
; #pragma unroll
;             for (int i = 0; i < 4; ++i) { u32x2 o; o.x = epi::pk4_fp8(v[h][0][i] * s[0], v[h][1][i] * s[1], v[h][2][i] * s[2], v[h][3][i] * s[3]); o.y = epi::pk4_fp8(v[h][4][i] * s[4], v[h][5][i] * s[5], v[h][6][i] * s[6], v[h][7][i] * s[7]);
;                 __builtin_nontemporal_store(o, (u32x2*)(t.dst + (size_t)(32 * h + 4 * n4 + i) * t.ldwt + 8 * kr)); }
	v_mul_f32_e32 v160, 0x43800000, v128
	v_mul_f32_e32 v161, 0x43800000, v129
	v_mul_f32_e32 v162, 0x43800000, v130
	v_mul_f32_e32 v163, 0x43800000, v131
	v_mul_f32_e32 v164, 0x43800000, v132
	v_mul_f32_e32 v165, 0x43800000, v133
	v_mul_f32_e32 v166, 0x43800000, v134
	v_mul_f32_e32 v167, 0x43800000, v135
	v_mul_f32_e32 v168, 0x43800000, v136
	v_mul_f32_e32 v169, 0x43800000, v137
	v_mul_f32_e32 v170, 0x43800000, v138
	v_mul_f32_e32 v171, 0x43800000, v139
	v_mul_f32_e32 v172, 0x43800000, v140
	v_mul_f32_e32 v173, 0x43800000, v141
	v_mul_f32_e32 v174, 0x43800000, v142
	v_mul_f32_e32 v175, 0x43800000, v143
	v_pk_mul_f32 v[0:1], v[0:1], v[160:161] op_sel:[0,0] op_sel_hi:[1,0]
	v_pk_mul_f32 v[2:3], v[2:3], v[160:161] op_sel:[0,0] op_sel_hi:[1,0]
	v_pk_mul_f32 v[4:5], v[4:5], v[160:161] op_sel:[0,1] op_sel_hi:[1,1]
	v_pk_mul_f32 v[6:7], v[6:7], v[160:161] op_sel:[0,1] op_sel_hi:[1,1]
	v_pk_mul_f32 v[8:9], v[8:9], v[162:163] op_sel:[0,0] op_sel_hi:[1,0]
	v_pk_mul_f32 v[10:11], v[10:11], v[162:163] op_sel:[0,0] op_sel_hi:[1,0]
	v_pk_mul_f32 v[12:13], v[12:13], v[162:163] op_sel:[0,1] op_sel_hi:[1,1]
	v_pk_mul_f32 v[14:15], v[14:15], v[162:163] op_sel:[0,1] op_sel_hi:[1,1]
	v_pk_mul_f32 v[16:17], v[16:17], v[164:165] op_sel:[0,0] op_sel_hi:[1,0]
	v_pk_mul_f32 v[18:19], v[18:19], v[164:165] op_sel:[0,0] op_sel_hi:[1,0]
	v_pk_mul_f32 v[20:21], v[20:21], v[164:165] op_sel:[0,1] op_sel_hi:[1,1]
	v_pk_mul_f32 v[22:23], v[22:23], v[164:165] op_sel:[0,1] op_sel_hi:[1,1]
	v_pk_mul_f32 v[24:25], v[24:25], v[166:167] op_sel:[0,0] op_sel_hi:[1,0]
	v_pk_mul_f32 v[26:27], v[26:27], v[166:167] op_sel:[0,0] op_sel_hi:[1,0]
	v_pk_mul_f32 v[28:29], v[28:29], v[166:167] op_sel:[0,1] op_sel_hi:[1,1]
	v_pk_mul_f32 v[30:31], v[30:31], v[166:167] op_sel:[0,1] op_sel_hi:[1,1]
	v_pk_mul_f32 v[32:33], v[32:33], v[168:169] op_sel:[0,0] op_sel_hi:[1,0]
	v_pk_mul_f32 v[34:35], v[34:35], v[168:169] op_sel:[0,0] op_sel_hi:[1,0]
	v_pk_mul_f32 v[36:37], v[36:37], v[168:169] op_sel:[0,1] op_sel_hi:[1,1]
	v_pk_mul_f32 v[38:39], v[38:39], v[168:169] op_sel:[0,1] op_sel_hi:[1,1]
	v_pk_mul_f32 v[40:41], v[40:41], v[170:171] op_sel:[0,0] op_sel_hi:[1,0]
	v_pk_mul_f32 v[42:43], v[42:43], v[170:171] op_sel:[0,0] op_sel_hi:[1,0]
	v_pk_mul_f32 v[44:45], v[44:45], v[170:171] op_sel:[0,1] op_sel_hi:[1,1]
	v_pk_mul_f32 v[46:47], v[46:47], v[170:171] op_sel:[0,1] op_sel_hi:[1,1]
	v_pk_mul_f32 v[48:49], v[48:49], v[172:173] op_sel:[0,0] op_sel_hi:[1,0]
	v_pk_mul_f32 v[50:51], v[50:51], v[172:173] op_sel:[0,0] op_sel_hi:[1,0]
	v_pk_mul_f32 v[52:53], v[52:53], v[172:173] op_sel:[0,1] op_sel_hi:[1,1]
	v_pk_mul_f32 v[54:55], v[54:55], v[172:173] op_sel:[0,1] op_sel_hi:[1,1]
	v_pk_mul_f32 v[56:57], v[56:57], v[174:175] op_sel:[0,0] op_sel_hi:[1,0]
	v_pk_mul_f32 v[58:59], v[58:59], v[174:175] op_sel:[0,0] op_sel_hi:[1,0]
	v_pk_mul_f32 v[60:61], v[60:61], v[174:175] op_sel:[0,1] op_sel_hi:[1,1]
	v_pk_mul_f32 v[62:63], v[62:63], v[174:175] op_sel:[0,1] op_sel_hi:[1,1]
	v_med3_f32 v0, v0, s33, v225
	v_med3_f32 v1, v1, s33, v225
	v_med3_f32 v2, v2, s33, v225
	v_med3_f32 v3, v3, s33, v225
	v_med3_f32 v4, v4, s33, v225
	v_med3_f32 v5, v5, s33, v225
	v_med3_f32 v6, v6, s33, v225
	v_med3_f32 v7, v7, s33, v225
	v_med3_f32 v8, v8, s33, v225
	v_med3_f32 v9, v9, s33, v225
	v_med3_f32 v10, v10, s33, v225
	v_med3_f32 v11, v11, s33, v225
	v_med3_f32 v12, v12, s33, v225
	v_med3_f32 v13, v13, s33, v225
	v_med3_f32 v14, v14, s33, v225
	v_med3_f32 v15, v15, s33, v225
	v_med3_f32 v16, v16, s33, v225
	v_med3_f32 v17, v17, s33, v225
	v_med3_f32 v18, v18, s33, v225
	v_med3_f32 v19, v19, s33, v225
	v_med3_f32 v20, v20, s33, v225
	v_med3_f32 v21, v21, s33, v225
	v_med3_f32 v22, v22, s33, v225
	v_med3_f32 v23, v23, s33, v225
	v_med3_f32 v24, v24, s33, v225
	v_med3_f32 v25, v25, s33, v225
	v_med3_f32 v26, v26, s33, v225
	v_med3_f32 v27, v27, s33, v225
	v_med3_f32 v28, v28, s33, v225
	v_med3_f32 v29, v29, s33, v225
	v_med3_f32 v30, v30, s33, v225
	v_med3_f32 v31, v31, s33, v225
	v_med3_f32 v32, v32, s33, v225
	v_med3_f32 v33, v33, s33, v225
	v_med3_f32 v34, v34, s33, v225
	v_med3_f32 v35, v35, s33, v225
	v_med3_f32 v36, v36, s33, v225
	v_med3_f32 v37, v37, s33, v225
	v_med3_f32 v38, v38, s33, v225
	v_med3_f32 v39, v39, s33, v225
	v_med3_f32 v40, v40, s33, v225
	v_med3_f32 v41, v41, s33, v225
	v_med3_f32 v42, v42, s33, v225
	v_med3_f32 v43, v43, s33, v225
	v_med3_f32 v44, v44, s33, v225
	v_med3_f32 v45, v45, s33, v225
	v_med3_f32 v46, v46, s33, v225
	v_med3_f32 v47, v47, s33, v225
	v_med3_f32 v48, v48, s33, v225
	v_med3_f32 v49, v49, s33, v225
	v_med3_f32 v50, v50, s33, v225
	v_med3_f32 v51, v51, s33, v225
	v_med3_f32 v52, v52, s33, v225
	v_med3_f32 v53, v53, s33, v225
	v_med3_f32 v54, v54, s33, v225
	v_med3_f32 v55, v55, s33, v225
	v_med3_f32 v56, v56, s33, v225
	v_med3_f32 v57, v57, s33, v225
	v_med3_f32 v58, v58, s33, v225
	v_med3_f32 v59, v59, s33, v225
	v_med3_f32 v60, v60, s33, v225
	v_med3_f32 v61, v61, s33, v225
	v_med3_f32 v62, v62, s33, v225
	v_med3_f32 v63, v63, s33, v225
	v_cvt_pk_fp8_f32 v226, v0, v4
	v_cvt_pk_fp8_f32 v227, v16, v20
	v_cvt_pk_fp8_f32 v228, v32, v36
	v_cvt_pk_fp8_f32 v229, v48, v52
	v_cvt_pk_fp8_f32 v226, v8, v12 op_sel:[0,0,1]
	v_cvt_pk_fp8_f32 v227, v24, v28 op_sel:[0,0,1]
	v_cvt_pk_fp8_f32 v228, v40, v44 op_sel:[0,0,1]
	v_cvt_pk_fp8_f32 v229, v56, v60 op_sel:[0,0,1]
	s_nop 0
	global_store_dwordx4 v223, v[226:229], s[38:39] nt
	v_cvt_pk_fp8_f32 v230, v1, v5
	v_cvt_pk_fp8_f32 v231, v17, v21
	v_cvt_pk_fp8_f32 v232, v33, v37
	v_cvt_pk_fp8_f32 v233, v49, v53
	v_cvt_pk_fp8_f32 v230, v9, v13 op_sel:[0,0,1]
	v_cvt_pk_fp8_f32 v231, v25, v29 op_sel:[0,0,1]
	v_cvt_pk_fp8_f32 v232, v41, v45 op_sel:[0,0,1]
	v_cvt_pk_fp8_f32 v233, v57, v61 op_sel:[0,0,1]
	v_add_u32_e32 v238, 0x800, v223
	global_store_dwordx4 v238, v[230:233], s[38:39] nt
	v_cvt_pk_fp8_f32 v226, v2, v6
	v_cvt_pk_fp8_f32 v227, v18, v22
	v_cvt_pk_fp8_f32 v228, v34, v38
	v_cvt_pk_fp8_f32 v229, v50, v54
	v_cvt_pk_fp8_f32 v226, v10, v14 op_sel:[0,0,1]
	v_cvt_pk_fp8_f32 v227, v26, v30 op_sel:[0,0,1]
	v_cvt_pk_fp8_f32 v228, v42, v46 op_sel:[0,0,1]
	v_cvt_pk_fp8_f32 v229, v58, v62 op_sel:[0,0,1]
	v_add_u32_e32 v238, 0x1000, v223
	global_store_dwordx4 v238, v[226:229], s[38:39] nt
	v_cvt_pk_fp8_f32 v230, v3, v7
	v_cvt_pk_fp8_f32 v231, v19, v23
	v_cvt_pk_fp8_f32 v232, v35, v39
	v_cvt_pk_fp8_f32 v233, v51, v55
	v_cvt_pk_fp8_f32 v230, v11, v15 op_sel:[0,0,1]
	v_cvt_pk_fp8_f32 v231, v27, v31 op_sel:[0,0,1]
	v_cvt_pk_fp8_f32 v232, v43, v47 op_sel:[0,0,1]
	v_cvt_pk_fp8_f32 v233, v59, v63 op_sel:[0,0,1]
	v_add_u32_e32 v238, 0x1800, v223
	global_store_dwordx4 v238, v[230:233], s[38:39] nt
	s_mov_b32 s27, 1
	s_mov_b32 s30, 14
